# speedup vs baseline: 1.0119x; 1.0119x over previous
.LBB2_10:
	v_mov_b32_e32 v11, v0
	s_waitcnt lgkmcnt(0)
	s_barrier
	s_lshl_b32 s8, s18, 7
	s_waitcnt vmcnt(7)
	v_add_u32_e32 v2, 0xffffff00, v11
	v_lshlrev_b32_e32 v3, 3, v11
	v_and_b32_e32 v3, 56, v3
	v_mov_b32_e32 v4, 0x11000
	v_lshrrev_b32_e32 v12, 3, v2
	v_ashrrev_i32_e32 v2, 3, v2
	s_movk_i32 s10, 0xffc0
	s_or_b32 s8, s8, s17
	v_lshl_or_b32 v10, v3, 1, v4
	v_bfi_b32 v7, s10, v2, v12
	s_movk_i32 s11, 0x90
	v_or_b32_e32 v6, s8, v3
	v_mad_u64_u32 v[2:3], s[8:9], v7, s11, v[10:11]
	ds_read_b128 v[2:5], v2 offset:18432
	v_lshlrev_b32_e32 v14, 1, v6
	v_lshl_add_u32 v13, v7, 8, v14
	v_lshrrev_b32_e32 v15, 3, v11
	v_ashrrev_i32_e32 v6, 3, v11
	s_waitcnt lgkmcnt(0)
	buffer_store_dwordx4 v[2:5], v13, s[4:7], 0 offen sc1
	v_bfi_b32 v16, s10, v6, v15
	v_mad_u64_u32 v[6:7], s[8:9], v16, s11, v[10:11]
	v_add_u32_e32 v2, 0x100, v11
	v_ashrrev_i32_e32 v2, 3, v2
	v_bfi_b32 v17, s10, v2, v12
	v_mad_u64_u32 v[2:3], s[8:9], v17, s11, v[10:11]
	v_add_u32_e32 v11, 0x200, v11
	v_ashrrev_i32_e32 v11, 3, v11
	ds_read_b128 v[6:9], v6 offset:18432
	v_bfi_b32 v15, s10, v11, v15
	ds_read_b128 v[2:5], v2 offset:18432
	v_mad_u64_u32 v[10:11], s[8:9], v15, s11, v[10:11]
	ds_read_b128 v[10:13], v10 offset:18432
	v_lshl_add_u32 v16, v16, 8, v14
	s_waitcnt lgkmcnt(2)
	buffer_store_dwordx4 v[6:9], v16, s[4:7], 0 offen sc1
	s_nop 1
	v_lshl_add_u32 v6, v17, 8, v14
	s_waitcnt lgkmcnt(1)
	buffer_store_dwordx4 v[2:5], v6, s[4:7], 0 offen sc1
	s_nop 1
	v_lshl_add_u32 v2, v15, 8, v14
	s_waitcnt lgkmcnt(0)
	buffer_store_dwordx4 v[10:13], v2, s[4:7], 0 offen sc1
	s_mov_b64 s[2:3], 0
.LBB2_17:
	s_and_b64 vcc, exec, s[2:3]
	s_cbranch_vccz .LBB2_27
	s_load_dwordx2 s[46:47], s[0:1], 0x90
	s_lshr_b32 s50, s15, 7
	s_bfe_u32 s51, s15, 0x10006
	s_and_b32 s48, s12, 7
	s_lshl_b32 s48, s48, 8
	s_lshl_b32 s49, s14, 6
	s_or_b32 s48, s48, s49
	s_lshl_b32 s49, s51, 5
	s_or_b32 s48, s48, s49
	s_lshl_b32 s49, s51, 7
	s_add_i32 s49, s49, 0x1e400
	v_mov_b32_e32 v240, 0x64646464
	s_mov_b32 s42, 0x4010400
	s_mov_b32 s43, 0x4030402
	s_load_dwordx2 s[2:3], s[0:1], 0x70
	s_load_dwordx4 s[4:7], s[0:1], 0x40
	s_load_dwordx2 s[36:37], s[0:1], 0x60
	s_lshr_b32 s11, s15, 7
	s_lshl_b32 s8, s12, 3
	s_or_b32 s8, s11, s8
	s_ashr_i32 s9, s8, 31
	s_bfe_u32 s10, s15, 0x10006
	s_lshl_b64 s[12:13], s[8:9], 12
	v_and_b32_e32 v156, 63, v0
	s_waitcnt lgkmcnt(0)
	s_add_u32 s12, s2, s12
	s_addc_u32 s13, s3, s13
	v_lshlrev_b32_e32 v24, 2, v0
	v_and_b32_e32 v24, 0xfc, v24
	v_lshl_or_b32 v24, s14, 8, v24
	global_load_dword v27, v24, s[36:37]
	v_lshlrev_b32_e32 v1, 3, v156
	global_load_dwordx2 v[154:155], v1, s[12:13]
	global_load_dwordx2 v[150:151], v1, s[12:13] offset:512
	global_load_dwordx2 v[146:147], v1, s[12:13] offset:1024
	global_load_dwordx2 v[142:143], v1, s[12:13] offset:1536
	global_load_dwordx2 v[152:153], v1, s[12:13] offset:2048
	global_load_dwordx2 v[148:149], v1, s[12:13] offset:2560
	global_load_dwordx2 v[144:145], v1, s[12:13] offset:3072
	global_load_dwordx2 v[140:141], v1, s[12:13] offset:3584
	s_lshl_b32 s9, s14, 10
	s_lshl_b32 s12, s10, 9
	s_or_b32 s9, s12, s9
	v_or_b32_e32 v1, s9, v156
	v_lshlrev_b32_e32 v2, 4, v1
	v_mov_b32_e32 v3, 0
	v_lshl_add_u64 v[4:5], s[4:5], 0, v[2:3]
	s_movk_i32 s9, 0x1000
	v_add_co_u32_e32 v4, vcc, s9, v4
	v_lshlrev_b32_e32 v1, 2, v0
	s_nop 0
	v_addc_co_u32_e32 v5, vcc, 0, v5, vcc
	global_load_dwordx4 v[86:89], v[4:5], off
	global_load_dwordx4 v[78:81], v[4:5], off offset:1024
	global_load_dwordx4 v[70:73], v[4:5], off offset:2048
	global_load_dwordx4 v[66:69], v[4:5], off offset:3072
	global_load_dwordx4 v[122:125], v2, s[4:5]
	global_load_dwordx4 v[126:129], v2, s[6:7]
	global_load_dwordx4 v[114:117], v2, s[4:5] offset:1024
	global_load_dwordx4 v[118:121], v2, s[6:7] offset:1024
	global_load_dwordx4 v[106:109], v2, s[4:5] offset:2048
	global_load_dwordx4 v[110:113], v2, s[6:7] offset:2048
	global_load_dwordx4 v[98:101], v2, s[4:5] offset:3072
	global_load_dwordx4 v[102:105], v2, s[6:7] offset:3072
	v_lshl_add_u64 v[4:5], s[6:7], 0, v[2:3]
	v_add_co_u32_e32 v2, vcc, 0x1000, v4
	s_nop 1
	v_addc_co_u32_e32 v3, vcc, 0, v5, vcc
	global_load_dwordx4 v[94:97], v[2:3], off
	global_load_dwordx4 v[90:93], v[2:3], off offset:1024
	global_load_dwordx4 v[82:85], v[2:3], off offset:2048
	global_load_dwordx4 v[74:77], v[2:3], off offset:3072
	v_cmp_gt_u32_e32 vcc, 64, v0
	s_and_saveexec_b64 s[4:5], vcc
	s_cbranch_execz .LBB2_20
	v_add_u32_e32 v3, 0x1ee00, v1
	s_waitcnt vmcnt(24)
	ds_write_b32 v3, v27

.LBB2_24:
	s_or_b64 exec, exec, s[0:1]
	v_and_b32_e32 v1, 31, v0
	v_lshlrev_b32_e32 v2, 2, v1
	v_lshl_or_b32 v2, s10, 7, v2
	v_or_b32_e32 v2, 0x1ee00, v2
	v_lshrrev_b32_e32 v158, 5, v156
	s_waitcnt lgkmcnt(0)
	s_barrier
	v_lshlrev_b32_e32 v250, 4, v158
	v_lshl_or_b32 v250, s10, 7, v250
	v_or_b32_e32 v254, 0x1ee00, v250
	ds_read_b128 v[168:171], v254 offset:0
	ds_read_b128 v[172:175], v254 offset:32
	ds_read_b128 v[176:179], v254 offset:64
	ds_read_b128 v[180:183], v254 offset:96
	v_bfe_u32 v255, v156, 2, 2
	v_lshl_add_u32 v250, v255, 2, v250
	v_add_u32_e32 v250, 0x1e400, v250
	s_waitcnt lgkmcnt(0)
	s_barrier
	ds_read_b32 v157, v2
	v_mul_u32_u24_e32 v2, 0x88, v1
	s_mul_i32 s0, s11, 0x4400
	v_lshlrev_b32_e32 v2, 1, v2
	v_lshlrev_b32_e32 v3, 4, v158
	v_mov_b32_e32 v138, v0
	v_add3_u32 v159, s0, v2, v3
	ds_read_b128 v[2:5], v159
	ds_read_b128 v[18:21], v159 offset:8704
	ds_read_b128 v[130:133], v159 offset:32
	s_waitcnt vmcnt(10) lgkmcnt(2)
	v_mfma_f32_32x32x16_f16 v[50:65], v[2:5], v[126:129], 0
	s_mov_b32 s4, 0xc060c00
	s_mov_b32 s5, 0xe400
	s_mulk_i32 s11, 0x2400
	s_lshl_b32 s0, s10, 6
	s_or_b32 s0, s11, s0
	s_add_i32 s0, s0, 0x11000
	v_mul_u32_u24_e32 v251, 0x90, v1
	v_lshl_add_u32 v251, v158, 3, v251
	v_add_u32_e32 v251, s0, v251
	s_waitcnt lgkmcnt(1)
	v_mfma_f32_32x32x16_f16 v[34:49], v[18:21], v[126:129], 0
	s_or_b32 s0, s8, 2
	s_ashr_i32 s1, s0, 31
	s_lshl_b64 s[0:1], s[0:1], 12
	s_add_u32 s0, s2, s0
	s_addc_u32 s1, s3, s1
	v_cmp_gt_u32_e32 vcc, 32, v156
	v_mfma_f32_32x32x16_f16 v[2:17], v[122:125], v[2:5], v[168:183]
	v_mfma_f32_32x32x16_f16 v[18:33], v[122:125], v[18:21], v[168:183]
	ds_read_b128 v[134:137], v159 offset:8736
	ds_read_b128 v[160:163], v159 offset:64
	s_waitcnt vmcnt(8) lgkmcnt(2)
	v_mfma_f32_32x32x16_f16 v[50:65], v[130:133], v[118:121], v[50:65]
	s_waitcnt lgkmcnt(1)
	v_mfma_f32_32x32x16_f16 v[34:49], v[134:137], v[118:121], v[34:49]
	v_mfma_f32_32x32x16_f16 v[2:17], v[114:117], v[130:133], v[2:17]
	v_mfma_f32_32x32x16_f16 v[18:33], v[114:117], v[134:137], v[18:33]
	ds_read_b128 v[130:133], v159 offset:8768
	ds_read_b128 v[134:137], v159 offset:96
	s_waitcnt vmcnt(6) lgkmcnt(2)
	v_mfma_f32_32x32x16_f16 v[50:65], v[160:163], v[110:113], v[50:65]
	s_waitcnt lgkmcnt(1)
	v_mfma_f32_32x32x16_f16 v[34:49], v[130:133], v[110:113], v[34:49]
	v_mfma_f32_32x32x16_f16 v[2:17], v[106:109], v[160:163], v[2:17]
	v_mfma_f32_32x32x16_f16 v[18:33], v[106:109], v[130:133], v[18:33]
	ds_read_b128 v[130:133], v159 offset:8800
	ds_read_b128 v[160:163], v159 offset:128
	s_waitcnt vmcnt(4) lgkmcnt(2)
	v_mfma_f32_32x32x16_f16 v[50:65], v[134:137], v[102:105], v[50:65]
	s_waitcnt lgkmcnt(1)
	v_mfma_f32_32x32x16_f16 v[34:49], v[130:133], v[102:105], v[34:49]
	v_mfma_f32_32x32x16_f16 v[2:17], v[98:101], v[134:137], v[2:17]
	v_mfma_f32_32x32x16_f16 v[18:33], v[98:101], v[130:133], v[18:33]
	ds_read_b128 v[130:133], v159 offset:8832
	ds_read_b128 v[134:137], v159 offset:160
	s_waitcnt vmcnt(3) lgkmcnt(2)
	v_mfma_f32_32x32x16_f16 v[50:65], v[160:163], v[94:97], v[50:65]
	s_waitcnt lgkmcnt(1)
	v_mfma_f32_32x32x16_f16 v[34:49], v[130:133], v[94:97], v[34:49]
	v_mfma_f32_32x32x16_f16 v[2:17], v[86:89], v[160:163], v[2:17]
	v_mfma_f32_32x32x16_f16 v[18:33], v[86:89], v[130:133], v[18:33]
	ds_read_b128 v[130:133], v159 offset:8864
	ds_read_b128 v[160:163], v159 offset:192
	s_waitcnt vmcnt(2) lgkmcnt(2)
	v_mfma_f32_32x32x16_f16 v[50:65], v[134:137], v[90:93], v[50:65]
	s_waitcnt lgkmcnt(1)
	v_mfma_f32_32x32x16_f16 v[34:49], v[130:133], v[90:93], v[34:49]
	v_mfma_f32_32x32x16_f16 v[2:17], v[78:81], v[134:137], v[2:17]
	v_mfma_f32_32x32x16_f16 v[18:33], v[78:81], v[130:133], v[18:33]
	ds_read_b128 v[130:133], v159 offset:8896
	ds_read_b128 v[164:167], v159 offset:224
	s_waitcnt vmcnt(1) lgkmcnt(2)
	v_mfma_f32_32x32x16_f16 v[50:65], v[160:163], v[82:85], v[50:65]
	s_waitcnt lgkmcnt(1)
	v_mfma_f32_32x32x16_f16 v[34:49], v[130:133], v[82:85], v[34:49]
	v_mfma_f32_32x32x16_f16 v[2:17], v[70:73], v[160:163], v[2:17]
	v_mfma_f32_32x32x16_f16 v[18:33], v[70:73], v[130:133], v[18:33]
	v_lshlrev_b32_e32 v130, 3, v138
	v_and_b32_e32 v241, 0x1f8, v130
	global_load_dwordx2 v[138:139], v241, s[0:1]
	global_load_dwordx2 v[134:135], v241, s[0:1] offset:512
	global_load_dwordx2 v[132:133], v241, s[0:1] offset:1024
	global_load_dwordx2 v[130:131], v241, s[0:1] offset:1536
	global_load_dwordx2 v[136:137], v241, s[0:1] offset:2048
	s_waitcnt vmcnt(5) lgkmcnt(0)
	v_mfma_f32_32x32x16_f16 v[50:65], v[164:167], v[74:77], v[50:65]
	v_mfma_f32_32x32x16_f16 v[2:17], v[66:69], v[164:167], v[2:17]
	s_nop 10
	v_cvt_pk_f16_f32 v57, v56, v57
	v_cvt_pk_f16_f32 v56, v54, v55
	v_cvt_pk_f16_f32 v55, v52, v53
	v_cvt_pk_f16_f32 v54, v50, v51
	v_perm_b32 v50, v240, v154, s42
	v_perm_b32 v51, v240, v154, s43
	v_perm_b32 v52, v240, v155, s42
	v_perm_b32 v53, v240, v155, s43
	v_pk_add_f16 v50, v50, s5 op_sel_hi:[1,0]
	v_pk_add_f16 v51, v51, s5 op_sel_hi:[1,0]
	v_pk_add_f16 v52, v52, s5 op_sel_hi:[1,0]
	v_pk_add_f16 v53, v53, s5 op_sel_hi:[1,0]
	v_cvt_pk_f16_f32 v65, v64, v65
	v_cvt_pk_f16_f32 v64, v62, v63
	v_cvt_pk_f16_f32 v63, v60, v61
	v_cvt_pk_f16_f32 v62, v58, v59
	v_mfma_f32_32x32x16_f16 v[2:17], v[54:57], v[50:53], v[2:17]
	v_perm_b32 v58, v240, v150, s42
	v_perm_b32 v59, v240, v150, s43
	v_perm_b32 v60, v240, v151, s42
	v_perm_b32 v61, v240, v151, s43
	v_pk_add_f16 v58, v58, s5 op_sel_hi:[1,0]
	v_pk_add_f16 v59, v59, s5 op_sel_hi:[1,0]
	v_pk_add_f16 v60, v60, s5 op_sel_hi:[1,0]
	v_pk_add_f16 v61, v61, s5 op_sel_hi:[1,0]
	s_nop 1
	v_mfma_f32_32x32x16_f16 v[2:17], v[62:65], v[58:61], v[2:17]
	ds_read_b128 v[160:163], v159 offset:8928
	v_perm_b32 v155, v240, v152, s43
	v_perm_b32 v164, v240, v153, s42
	s_waitcnt lgkmcnt(0)
	v_mfma_f32_32x32x16_f16 v[18:33], v[66:69], v[160:163], v[18:33]
	v_perm_b32 v154, v240, v152, s42
	v_perm_b32 v165, v240, v153, s43
	v_pk_add_f16 v152, v154, s5 op_sel_hi:[1,0]
	v_pk_add_f16 v153, v155, s5 op_sel_hi:[1,0]
	v_pk_add_f16 v154, v164, s5 op_sel_hi:[1,0]
	v_pk_add_f16 v155, v165, s5 op_sel_hi:[1,0]
	v_mfma_f32_32x32x16_f16 v[34:49], v[160:163], v[74:77], v[34:49]
	v_perm_b32 v151, v240, v148, s43
	v_perm_b32 v164, v240, v149, s42
	v_mfma_f32_32x32x16_f16 v[18:33], v[54:57], v[152:155], v[18:33]
	v_perm_b32 v150, v240, v148, s42
	v_perm_b32 v165, v240, v149, s43
	v_pk_add_f16 v148, v150, s5 op_sel_hi:[1,0]
	v_pk_add_f16 v149, v151, s5 op_sel_hi:[1,0]
	v_pk_add_f16 v150, v164, s5 op_sel_hi:[1,0]
	v_pk_add_f16 v151, v165, s5 op_sel_hi:[1,0]
	s_nop 2
	v_cvt_pk_f16_f32 v41, v40, v41
	v_cvt_pk_f16_f32 v40, v38, v39
	v_cvt_pk_f16_f32 v38, v34, v35
	v_cvt_pk_f16_f32 v39, v36, v37
	v_mfma_f32_32x32x16_f16 v[18:33], v[62:65], v[148:151], v[18:33]
	v_perm_b32 v34, v240, v146, s42
	v_perm_b32 v35, v240, v146, s43
	v_perm_b32 v36, v240, v147, s42
	v_perm_b32 v37, v240, v147, s43
	v_pk_add_f16 v34, v34, s5 op_sel_hi:[1,0]
	v_pk_add_f16 v35, v35, s5 op_sel_hi:[1,0]
	v_pk_add_f16 v36, v36, s5 op_sel_hi:[1,0]
	v_pk_add_f16 v37, v37, s5 op_sel_hi:[1,0]
	v_perm_b32 v146, v240, v144, s42
	v_perm_b32 v144, v240, v144, s43
	v_perm_b32 v147, v240, v145, s42
	v_perm_b32 v53, v240, v145, s43
	v_pk_add_f16 v50, v146, s5 op_sel_hi:[1,0]
	v_pk_add_f16 v51, v144, s5 op_sel_hi:[1,0]
	v_pk_add_f16 v52, v147, s5 op_sel_hi:[1,0]
	v_pk_add_f16 v53, v53, s5 op_sel_hi:[1,0]
	v_cvt_pk_f16_f32 v49, v48, v49
	v_cvt_pk_f16_f32 v48, v46, v47
	v_cvt_pk_f16_f32 v47, v44, v45
	v_mfma_f32_32x32x16_f16 v[2:17], v[38:41], v[34:37], v[2:17]
	v_cvt_pk_f16_f32 v46, v42, v43
	v_mfma_f32_32x32x16_f16 v[18:33], v[38:41], v[50:53], v[18:33]
	v_perm_b32 v34, v240, v140, s42
	v_perm_b32 v35, v240, v140, s43
	v_perm_b32 v36, v240, v141, s42
	v_perm_b32 v37, v240, v141, s43
	v_perm_b32 v42, v240, v142, s42
	v_perm_b32 v43, v240, v142, s43
	v_perm_b32 v44, v240, v143, s42
	v_perm_b32 v45, v240, v143, s43
	v_pk_add_f16 v34, v34, s5 op_sel_hi:[1,0]
	v_pk_add_f16 v35, v35, s5 op_sel_hi:[1,0]
	v_pk_add_f16 v36, v36, s5 op_sel_hi:[1,0]
	v_pk_add_f16 v37, v37, s5 op_sel_hi:[1,0]
	v_pk_add_f16 v42, v42, s5 op_sel_hi:[1,0]
	v_pk_add_f16 v43, v43, s5 op_sel_hi:[1,0]
	v_pk_add_f16 v44, v44, s5 op_sel_hi:[1,0]
	v_pk_add_f16 v45, v45, s5 op_sel_hi:[1,0]
	v_mfma_f32_32x32x16_f16 v[18:33], v[46:49], v[34:37], v[18:33]
	global_load_dwordx2 v[154:155], v241, s[0:1] offset:2560
	global_load_dwordx2 v[152:153], v241, s[0:1] offset:3072
	global_load_dwordx2 v[150:151], v241, s[0:1] offset:3584
	v_mov_b32_e32 v148, v0
	s_or_b32 s0, s8, 4
	s_ashr_i32 s1, s0, 31
	s_lshl_b64 s[0:1], s[0:1], 12
	v_mfma_f32_32x32x16_f16 v[2:17], v[46:49], v[42:45], v[2:17]
	s_nop 7
	s_nop 4
	v_cvt_pk_f16_f32 v254, v2, v3
	v_cvt_pk_f16_f32 v255, v4, v5
	ds_write_b64 v251, v[254:255] offset:0
	v_mov_b32_e32 v222, v2
	v_mov_b32_e32 v223, v3
	v_pk_mul_f32 v[194:195], v[2:3], v[2:3]
	v_mov_b32_e32 v220, v4
	v_mov_b32_e32 v221, v5
	v_pk_mul_f32 v[192:193], v[4:5], v[4:5]
	v_cvt_pk_f16_f32 v252, v6, v7
	v_cvt_pk_f16_f32 v253, v8, v9
	ds_write_b64 v251, v[252:253] offset:16
	v_mov_b32_e32 v218, v6
	v_mov_b32_e32 v219, v7
	v_pk_mul_f32 v[184:185], v[6:7], v[6:7]
	v_mov_b32_e32 v216, v8
	v_mov_b32_e32 v217, v9
	v_pk_mul_f32 v[166:167], v[8:9], v[8:9]
	v_cvt_pk_f16_f32 v254, v10, v11
	v_cvt_pk_f16_f32 v255, v12, v13
	ds_write_b64 v251, v[254:255] offset:32
	v_mov_b32_e32 v214, v10
	v_mov_b32_e32 v215, v11
	v_pk_mul_f32 v[164:165], v[10:11], v[10:11]
	v_mov_b32_e32 v204, v12
	v_mov_b32_e32 v205, v13
	v_pk_mul_f32 v[162:163], v[12:13], v[12:13]
	v_cvt_pk_f16_f32 v252, v14, v15
	v_cvt_pk_f16_f32 v253, v16, v17
	ds_write_b64 v251, v[252:253] offset:48
	v_mov_b32_e32 v202, v14
	v_mov_b32_e32 v203, v15
	v_pk_mul_f32 v[160:161], v[14:15], v[14:15]
	v_mov_b32_e32 v196, v16
	v_mov_b32_e32 v197, v17
	v_pk_mul_f32 v[156:157], v[16:17], v[16:17]
	v_cvt_pk_f16_f32 v254, v18, v19
	v_cvt_pk_f16_f32 v255, v20, v21
	ds_write_b64 v251, v[254:255] offset:4608
	v_pk_add_f32 v[222:223], v[222:223], v[18:19]
	v_pk_fma_f32 v[194:195], v[18:19], v[18:19], v[194:195]
	v_pk_add_f32 v[220:221], v[220:221], v[20:21]
	v_pk_fma_f32 v[192:193], v[20:21], v[20:21], v[192:193]
	v_cvt_pk_f16_f32 v252, v22, v23
	v_cvt_pk_f16_f32 v253, v24, v25
	ds_write_b64 v251, v[252:253] offset:4624
	v_pk_add_f32 v[218:219], v[218:219], v[22:23]
	v_pk_fma_f32 v[184:185], v[22:23], v[22:23], v[184:185]
	v_pk_add_f32 v[216:217], v[216:217], v[24:25]
	v_pk_fma_f32 v[166:167], v[24:25], v[24:25], v[166:167]
	v_cvt_pk_f16_f32 v254, v26, v27
	v_cvt_pk_f16_f32 v255, v28, v29
	ds_write_b64 v251, v[254:255] offset:4640
	v_pk_add_f32 v[214:215], v[214:215], v[26:27]
	v_pk_fma_f32 v[164:165], v[26:27], v[26:27], v[164:165]
	v_pk_add_f32 v[204:205], v[204:205], v[28:29]
	v_pk_fma_f32 v[162:163], v[28:29], v[28:29], v[162:163]
	v_cvt_pk_f16_f32 v252, v30, v31
	v_cvt_pk_f16_f32 v253, v32, v33
	ds_write_b64 v251, v[252:253] offset:4656
	v_pk_add_f32 v[202:203], v[202:203], v[30:31]
	v_pk_fma_f32 v[160:161], v[30:31], v[30:31], v[160:161]
	v_pk_add_f32 v[196:197], v[196:197], v[32:33]
	v_pk_fma_f32 v[156:157], v[32:33], v[32:33], v[156:157]
	s_nop 3
	s_nop 0
	s_waitcnt lgkmcnt(0)
	s_barrier
	s_nop 4
	ds_read_b128 v[2:5], v159 offset:34816
	ds_read_b128 v[18:21], v159 offset:43520
	ds_read_b128 v[140:143], v159 offset:34848
	ds_read_b128 v[144:147], v159 offset:43552
	s_waitcnt lgkmcnt(3)
	v_mfma_f32_32x32x16_f16 v[50:65], v[2:5], v[126:129], 0
	s_add_u32 s0, s2, s0
	s_addc_u32 s1, s3, s1
	s_waitcnt lgkmcnt(2)
	v_mfma_f32_32x32x16_f16 v[34:49], v[18:21], v[126:129], 0
	v_mfma_f32_32x32x16_f16 v[2:17], v[122:125], v[2:5], v[168:183]
	v_mfma_f32_32x32x16_f16 v[18:33], v[122:125], v[18:21], v[168:183]
	ds_read_b128 v[242:245], v159 offset:34880
	ds_read_b128 v[246:249], v159 offset:43584
	s_waitcnt lgkmcnt(3)
	v_mfma_f32_32x32x16_f16 v[50:65], v[140:143], v[118:121], v[50:65]
	s_waitcnt lgkmcnt(2)
	v_mfma_f32_32x32x16_f16 v[34:49], v[144:147], v[118:121], v[34:49]
	v_mfma_f32_32x32x16_f16 v[2:17], v[114:117], v[140:143], v[2:17]
	v_mfma_f32_32x32x16_f16 v[18:33], v[114:117], v[144:147], v[18:33]
	ds_read_b128 v[140:143], v159 offset:34912
	ds_read_b128 v[144:147], v159 offset:43616
	s_waitcnt lgkmcnt(3)
	v_mfma_f32_32x32x16_f16 v[50:65], v[242:245], v[110:113], v[50:65]
	s_waitcnt lgkmcnt(2)
	v_mfma_f32_32x32x16_f16 v[34:49], v[246:249], v[110:113], v[34:49]
	v_mfma_f32_32x32x16_f16 v[2:17], v[106:109], v[242:245], v[2:17]
	v_mfma_f32_32x32x16_f16 v[18:33], v[106:109], v[246:249], v[18:33]
	ds_read_b128 v[242:245], v159 offset:34944
	ds_read_b128 v[246:249], v159 offset:43648
	s_waitcnt lgkmcnt(3)
	v_mfma_f32_32x32x16_f16 v[50:65], v[140:143], v[102:105], v[50:65]
	s_waitcnt lgkmcnt(2)
	v_mfma_f32_32x32x16_f16 v[34:49], v[144:147], v[102:105], v[34:49]
	v_mfma_f32_32x32x16_f16 v[2:17], v[98:101], v[140:143], v[2:17]
	v_mfma_f32_32x32x16_f16 v[18:33], v[98:101], v[144:147], v[18:33]
	ds_read_b128 v[186:189], v159 offset:34976
	ds_read_b128 v[206:209], v159 offset:43680
	s_waitcnt lgkmcnt(3)
	v_mfma_f32_32x32x16_f16 v[50:65], v[242:245], v[94:97], v[50:65]
	s_waitcnt lgkmcnt(2)
	v_mfma_f32_32x32x16_f16 v[34:49], v[246:249], v[94:97], v[34:49]
	v_mfma_f32_32x32x16_f16 v[2:17], v[86:89], v[242:245], v[2:17]
	v_mfma_f32_32x32x16_f16 v[18:33], v[86:89], v[246:249], v[18:33]
	ds_read_b128 v[140:143], v159 offset:35008
	ds_read_b128 v[144:147], v159 offset:43712
	s_waitcnt lgkmcnt(3)
	v_mfma_f32_32x32x16_f16 v[50:65], v[186:189], v[90:93], v[50:65]
	s_waitcnt lgkmcnt(2)
	v_mfma_f32_32x32x16_f16 v[34:49], v[206:209], v[90:93], v[34:49]
	v_mfma_f32_32x32x16_f16 v[2:17], v[78:81], v[186:189], v[2:17]
	v_mfma_f32_32x32x16_f16 v[18:33], v[78:81], v[206:209], v[18:33]
	ds_read_b128 v[186:189], v159 offset:35040
	ds_read_b128 v[206:209], v159 offset:43744
	s_waitcnt lgkmcnt(3)
	v_mfma_f32_32x32x16_f16 v[50:65], v[140:143], v[82:85], v[50:65]
	s_waitcnt lgkmcnt(2)
	v_mfma_f32_32x32x16_f16 v[34:49], v[144:147], v[82:85], v[34:49]
	v_mfma_f32_32x32x16_f16 v[2:17], v[70:73], v[140:143], v[2:17]
	v_lshlrev_b32_e32 v140, 3, v148
	v_and_b32_e32 v199, 0x1f8, v140
	global_load_dwordx2 v[148:149], v199, s[0:1]
	global_load_dwordx2 v[142:143], v199, s[0:1] offset:1024
	global_load_dwordx2 v[140:141], v199, s[0:1] offset:1536
	v_mfma_f32_32x32x16_f16 v[18:33], v[70:73], v[144:147], v[18:33]
	global_load_dwordx2 v[144:145], v199, s[0:1] offset:512
	global_load_dwordx2 v[146:147], v199, s[0:1] offset:2048
	s_waitcnt lgkmcnt(1)
	v_mfma_f32_32x32x16_f16 v[50:65], v[186:189], v[74:77], v[50:65]
	v_mfma_f32_32x32x16_f16 v[2:17], v[66:69], v[186:189], v[2:17]
	s_nop 10
	v_cvt_pk_f16_f32 v57, v56, v57
	v_cvt_pk_f16_f32 v56, v54, v55
	v_cvt_pk_f16_f32 v54, v50, v51
	s_waitcnt vmcnt(12)
	v_cvt_pk_f16_f32 v55, v52, v53
	s_waitcnt vmcnt(8)
	v_perm_b32 v50, v240, v138, s42
	v_perm_b32 v51, v240, v138, s43
	v_perm_b32 v52, v240, v139, s42
	v_perm_b32 v53, v240, v139, s43
	v_perm_b32 v139, v240, v136, s43
	v_pk_add_f16 v50, v50, s5 op_sel_hi:[1,0]
	v_pk_add_f16 v51, v51, s5 op_sel_hi:[1,0]
	v_pk_add_f16 v52, v52, s5 op_sel_hi:[1,0]
	v_pk_add_f16 v53, v53, s5 op_sel_hi:[1,0]
	v_perm_b32 v190, v240, v137, s42
	s_waitcnt lgkmcnt(0)
	v_mfma_f32_32x32x16_f16 v[18:33], v[66:69], v[206:209], v[18:33]
	v_perm_b32 v138, v240, v136, s42
	v_perm_b32 v191, v240, v137, s43
	v_pk_add_f16 v136, v138, s5 op_sel_hi:[1,0]
	v_pk_add_f16 v137, v139, s5 op_sel_hi:[1,0]
	v_pk_add_f16 v138, v190, s5 op_sel_hi:[1,0]
	v_pk_add_f16 v139, v191, s5 op_sel_hi:[1,0]
	v_cvt_pk_f16_f32 v65, v64, v65
	v_cvt_pk_f16_f32 v64, v62, v63
	v_cvt_pk_f16_f32 v63, v60, v61
	v_cvt_pk_f16_f32 v62, v58, v59
	v_mfma_f32_32x32x16_f16 v[34:49], v[206:209], v[74:77], v[34:49]
	v_mfma_f32_32x32x16_f16 v[2:17], v[54:57], v[50:53], v[2:17]
	s_waitcnt vmcnt(7)
	v_perm_b32 v58, v240, v134, s42
	v_perm_b32 v59, v240, v134, s43
	v_perm_b32 v60, v240, v135, s42
	v_perm_b32 v61, v240, v135, s43
	v_pk_add_f16 v58, v58, s5 op_sel_hi:[1,0]
	v_pk_add_f16 v59, v59, s5 op_sel_hi:[1,0]
	v_pk_add_f16 v60, v60, s5 op_sel_hi:[1,0]
	v_pk_add_f16 v61, v61, s5 op_sel_hi:[1,0]
	v_mfma_f32_32x32x16_f16 v[18:33], v[54:57], v[136:139], v[18:33]
	v_perm_b32 v134, v240, v154, s42
	v_perm_b32 v135, v240, v154, s43
	v_perm_b32 v154, v240, v155, s42
	v_perm_b32 v155, v240, v155, s43
	v_pk_add_f16 v210, v134, s5 op_sel_hi:[1,0]
	v_pk_add_f16 v211, v135, s5 op_sel_hi:[1,0]
	v_pk_add_f16 v212, v154, s5 op_sel_hi:[1,0]
	v_pk_add_f16 v213, v155, s5 op_sel_hi:[1,0]
	v_cvt_pk_f16_f32 v41, v40, v41
	v_cvt_pk_f16_f32 v40, v38, v39
	v_cvt_pk_f16_f32 v39, v36, v37
	v_cvt_pk_f16_f32 v38, v34, v35
	v_mfma_f32_32x32x16_f16 v[2:17], v[62:65], v[58:61], v[2:17]
	v_perm_b32 v34, v240, v132, s42
	v_perm_b32 v35, v240, v132, s43
	v_perm_b32 v36, v240, v133, s42
	v_perm_b32 v37, v240, v133, s43
	v_pk_add_f16 v34, v34, s5 op_sel_hi:[1,0]
	v_pk_add_f16 v35, v35, s5 op_sel_hi:[1,0]
	v_pk_add_f16 v36, v36, s5 op_sel_hi:[1,0]
	v_pk_add_f16 v37, v37, s5 op_sel_hi:[1,0]
	s_waitcnt vmcnt(6)
	v_mfma_f32_32x32x16_f16 v[18:33], v[62:65], v[210:213], v[18:33]
	v_perm_b32 v132, v240, v152, s42
	v_perm_b32 v133, v240, v152, s43
	v_perm_b32 v134, v240, v153, s42
	v_perm_b32 v53, v240, v153, s43
	v_pk_add_f16 v50, v132, s5 op_sel_hi:[1,0]
	v_pk_add_f16 v51, v133, s5 op_sel_hi:[1,0]
	v_pk_add_f16 v52, v134, s5 op_sel_hi:[1,0]
	v_pk_add_f16 v53, v53, s5 op_sel_hi:[1,0]
	v_cvt_pk_f16_f32 v49, v48, v49
	v_cvt_pk_f16_f32 v48, v46, v47
	v_cvt_pk_f16_f32 v47, v44, v45
	v_cvt_pk_f16_f32 v46, v42, v43
	v_mfma_f32_32x32x16_f16 v[2:17], v[38:41], v[34:37], v[2:17]
	v_perm_b32 v42, v240, v130, s42
	v_perm_b32 v43, v240, v130, s43
	v_perm_b32 v44, v240, v131, s42
	v_perm_b32 v45, v240, v131, s43
	v_pk_add_f16 v42, v42, s5 op_sel_hi:[1,0]
	v_pk_add_f16 v43, v43, s5 op_sel_hi:[1,0]
	v_pk_add_f16 v44, v44, s5 op_sel_hi:[1,0]
	v_pk_add_f16 v45, v45, s5 op_sel_hi:[1,0]
	s_waitcnt vmcnt(5)
	v_mfma_f32_32x32x16_f16 v[18:33], v[38:41], v[50:53], v[18:33]
	v_perm_b32 v34, v240, v150, s42
	v_perm_b32 v35, v240, v150, s43
	v_perm_b32 v36, v240, v151, s42
	v_perm_b32 v37, v240, v151, s43
	v_pk_add_f16 v34, v34, s5 op_sel_hi:[1,0]
	v_pk_add_f16 v35, v35, s5 op_sel_hi:[1,0]
	v_pk_add_f16 v36, v36, s5 op_sel_hi:[1,0]
	v_pk_add_f16 v37, v37, s5 op_sel_hi:[1,0]
	v_mfma_f32_32x32x16_f16 v[2:17], v[46:49], v[42:45], v[2:17]
	global_load_dwordx2 v[154:155], v199, s[0:1] offset:2560
	global_load_dwordx2 v[152:153], v199, s[0:1] offset:3072
	global_load_dwordx2 v[150:151], v199, s[0:1] offset:3584
	s_or_b32 s0, s8, 6
	s_ashr_i32 s1, s0, 31
	s_lshl_b64 s[0:1], s[0:1], 12
	s_add_u32 s0, s2, s0
	v_mfma_f32_32x32x16_f16 v[18:33], v[46:49], v[34:37], v[18:33]
	s_nop 7
	s_nop 4
	v_cvt_pk_f16_f32 v254, v2, v3
	v_cvt_pk_f16_f32 v255, v4, v5
	ds_write_b64 v251, v[254:255] offset:18432
	v_pk_add_f32 v[222:223], v[222:223], v[2:3]
	v_pk_fma_f32 v[194:195], v[2:3], v[2:3], v[194:195]
	v_pk_add_f32 v[220:221], v[220:221], v[4:5]
	v_pk_fma_f32 v[192:193], v[4:5], v[4:5], v[192:193]
	v_cvt_pk_f16_f32 v252, v6, v7
	v_cvt_pk_f16_f32 v253, v8, v9
	ds_write_b64 v251, v[252:253] offset:18448
	v_pk_add_f32 v[218:219], v[218:219], v[6:7]
	v_pk_fma_f32 v[184:185], v[6:7], v[6:7], v[184:185]
	v_pk_add_f32 v[216:217], v[216:217], v[8:9]
	v_pk_fma_f32 v[166:167], v[8:9], v[8:9], v[166:167]
	v_cvt_pk_f16_f32 v254, v10, v11
	v_cvt_pk_f16_f32 v255, v12, v13
	ds_write_b64 v251, v[254:255] offset:18464
	v_pk_add_f32 v[214:215], v[214:215], v[10:11]
	v_pk_fma_f32 v[164:165], v[10:11], v[10:11], v[164:165]
	v_pk_add_f32 v[204:205], v[204:205], v[12:13]
	v_pk_fma_f32 v[162:163], v[12:13], v[12:13], v[162:163]
	v_cvt_pk_f16_f32 v252, v14, v15
	v_cvt_pk_f16_f32 v253, v16, v17
	ds_write_b64 v251, v[252:253] offset:18480
	v_pk_add_f32 v[202:203], v[202:203], v[14:15]
	v_pk_fma_f32 v[160:161], v[14:15], v[14:15], v[160:161]
	v_pk_add_f32 v[196:197], v[196:197], v[16:17]
	v_pk_fma_f32 v[156:157], v[16:17], v[16:17], v[156:157]
	v_cvt_pk_f16_f32 v254, v18, v19
	v_cvt_pk_f16_f32 v255, v20, v21
	ds_write_b64 v251, v[254:255] offset:23040
	v_pk_add_f32 v[222:223], v[222:223], v[18:19]
	v_pk_fma_f32 v[194:195], v[18:19], v[18:19], v[194:195]
	v_pk_add_f32 v[220:221], v[220:221], v[20:21]
	v_pk_fma_f32 v[192:193], v[20:21], v[20:21], v[192:193]
	v_cvt_pk_f16_f32 v252, v22, v23
	v_cvt_pk_f16_f32 v253, v24, v25
	ds_write_b64 v251, v[252:253] offset:23056
	v_pk_add_f32 v[218:219], v[218:219], v[22:23]
	v_pk_fma_f32 v[184:185], v[22:23], v[22:23], v[184:185]
	v_pk_add_f32 v[216:217], v[216:217], v[24:25]
	v_pk_fma_f32 v[166:167], v[24:25], v[24:25], v[166:167]
	v_cvt_pk_f16_f32 v254, v26, v27
	v_cvt_pk_f16_f32 v255, v28, v29
	ds_write_b64 v251, v[254:255] offset:23072
	v_pk_add_f32 v[214:215], v[214:215], v[26:27]
	v_pk_fma_f32 v[164:165], v[26:27], v[26:27], v[164:165]
	v_pk_add_f32 v[204:205], v[204:205], v[28:29]
	v_pk_fma_f32 v[162:163], v[28:29], v[28:29], v[162:163]
	v_cvt_pk_f16_f32 v252, v30, v31
	v_cvt_pk_f16_f32 v253, v32, v33
	ds_write_b64 v251, v[252:253] offset:23088
	v_pk_add_f32 v[202:203], v[202:203], v[30:31]
	v_pk_fma_f32 v[160:161], v[30:31], v[30:31], v[160:161]
	v_pk_add_f32 v[196:197], v[196:197], v[32:33]
	v_pk_fma_f32 v[156:157], v[32:33], v[32:33], v[156:157]
	s_nop 3
	s_nop 0
	s_nop 0
	s_waitcnt lgkmcnt(0)
	s_barrier
	ds_read_b128 v[2:5], v159
	s_nop 2
	ds_read_b128 v[18:21], v159 offset:8704
	s_waitcnt lgkmcnt(1)
	v_mfma_f32_32x32x16_f16 v[50:65], v[2:5], v[126:129], 0
	v_lshlrev_b32_e32 v0, 3, v0
	s_addc_u32 s1, s3, s1
	v_and_b32_e32 v0, 0x1f8, v0
	global_load_dwordx2 v[138:139], v0, s[0:1]
	s_waitcnt lgkmcnt(0)
	v_mfma_f32_32x32x16_f16 v[34:49], v[18:21], v[126:129], 0
	v_mfma_f32_32x32x16_f16 v[2:17], v[122:125], v[2:5], v[168:183]
	v_mfma_f32_32x32x16_f16 v[18:33], v[122:125], v[18:21], v[168:183]
	ds_read_b128 v[130:133], v159 offset:32
	ds_read_b128 v[134:137], v159 offset:8736
	s_waitcnt lgkmcnt(1)
	v_mfma_f32_32x32x16_f16 v[50:65], v[130:133], v[118:121], v[50:65]
	s_waitcnt lgkmcnt(0)
	v_mfma_f32_32x32x16_f16 v[34:49], v[134:137], v[118:121], v[34:49]
	v_mfma_f32_32x32x16_f16 v[2:17], v[114:117], v[130:133], v[2:17]
	v_mfma_f32_32x32x16_f16 v[18:33], v[114:117], v[134:137], v[18:33]
	ds_read_b128 v[224:227], v159 offset:64
	ds_read_b128 v[228:231], v159 offset:8768
	ds_read_b128 v[130:133], v159 offset:96
	ds_read_b128 v[134:137], v159 offset:8800
	s_waitcnt lgkmcnt(3)
	v_mfma_f32_32x32x16_f16 v[50:65], v[224:227], v[110:113], v[50:65]
	s_waitcnt lgkmcnt(2)
	v_mfma_f32_32x32x16_f16 v[34:49], v[228:231], v[110:113], v[34:49]
	v_mfma_f32_32x32x16_f16 v[2:17], v[106:109], v[224:227], v[2:17]
	v_mfma_f32_32x32x16_f16 v[18:33], v[106:109], v[228:231], v[18:33]
	ds_read_b128 v[224:227], v159 offset:128
	ds_read_b128 v[228:231], v159 offset:8832
	s_waitcnt lgkmcnt(3)
	v_mfma_f32_32x32x16_f16 v[50:65], v[130:133], v[102:105], v[50:65]
	s_waitcnt lgkmcnt(2)
	v_mfma_f32_32x32x16_f16 v[34:49], v[134:137], v[102:105], v[34:49]
	v_mfma_f32_32x32x16_f16 v[2:17], v[98:101], v[130:133], v[2:17]
	v_mfma_f32_32x32x16_f16 v[18:33], v[98:101], v[134:137], v[18:33]
	ds_read_b128 v[130:133], v159 offset:160
	ds_read_b128 v[134:137], v159 offset:8864
	s_waitcnt lgkmcnt(3)
	v_mfma_f32_32x32x16_f16 v[50:65], v[224:227], v[94:97], v[50:65]
	s_waitcnt lgkmcnt(2)
	v_mfma_f32_32x32x16_f16 v[34:49], v[228:231], v[94:97], v[34:49]
	v_mfma_f32_32x32x16_f16 v[2:17], v[86:89], v[224:227], v[2:17]
	v_mfma_f32_32x32x16_f16 v[18:33], v[86:89], v[228:231], v[18:33]
	ds_read_b128 v[224:227], v159 offset:192
	ds_read_b128 v[228:231], v159 offset:8896
	s_waitcnt lgkmcnt(3)
	v_mfma_f32_32x32x16_f16 v[50:65], v[130:133], v[90:93], v[50:65]
	s_waitcnt lgkmcnt(2)
	v_mfma_f32_32x32x16_f16 v[34:49], v[134:137], v[90:93], v[34:49]
	v_mfma_f32_32x32x16_f16 v[2:17], v[78:81], v[130:133], v[2:17]
	v_mfma_f32_32x32x16_f16 v[18:33], v[78:81], v[134:137], v[18:33]
	ds_read_b128 v[232:235], v159 offset:224
	ds_read_b128 v[236:239], v159 offset:8928
	s_waitcnt lgkmcnt(3)
	v_mfma_f32_32x32x16_f16 v[50:65], v[224:227], v[82:85], v[50:65]
	global_load_dwordx2 v[134:135], v0, s[0:1] offset:512
	global_load_dwordx2 v[132:133], v0, s[0:1] offset:1024
	global_load_dwordx2 v[130:131], v0, s[0:1] offset:1536
	s_waitcnt lgkmcnt(2)
	v_mfma_f32_32x32x16_f16 v[34:49], v[228:231], v[82:85], v[34:49]
	global_load_dwordx2 v[136:137], v0, s[0:1] offset:2048
	v_mfma_f32_32x32x16_f16 v[2:17], v[70:73], v[224:227], v[2:17]
	v_mfma_f32_32x32x16_f16 v[18:33], v[70:73], v[228:231], v[18:33]
	s_waitcnt lgkmcnt(1)
	v_mfma_f32_32x32x16_f16 v[50:65], v[232:235], v[74:77], v[50:65]
	v_mfma_f32_32x32x16_f16 v[2:17], v[66:69], v[232:235], v[2:17]
	s_nop 10
	v_cvt_pk_f16_f32 v57, v56, v57
	v_cvt_pk_f16_f32 v56, v54, v55
	v_cvt_pk_f16_f32 v54, v50, v51
	s_waitcnt vmcnt(12)
	v_lshlrev_b32_e32 v50, 8, v148
	v_cvt_pk_f16_f32 v55, v52, v53
	v_perm_b32 v50, v50, v148, s4
	v_lshrrev_b32_e32 v51, 16, v148
	v_lshrrev_b32_e32 v52, 8, v148
	v_lshrrev_b32_e32 v53, 16, v149
	v_lshrrev_b32_e32 v148, 8, v149
	v_perm_b32 v51, v52, v51, s4
	v_lshlrev_b32_e32 v52, 8, v149
	v_perm_b32 v53, v148, v53, s4
	s_waitcnt vmcnt(8)
	v_perm_b32 v52, v52, v149, s4
	v_perm_b32 v149, v240, v146, s43
	v_perm_b32 v198, v240, v147, s42
	s_waitcnt lgkmcnt(0)
	v_mfma_f32_32x32x16_f16 v[18:33], v[66:69], v[236:239], v[18:33]
	v_or_b32_e32 v50, 0x64006400, v50
	v_or_b32_e32 v51, 0x64006400, v51
	v_or_b32_e32 v52, 0x64006400, v52
	v_or_b32_e32 v53, 0x64006400, v53
	v_pk_add_f16 v50, v50, s5 op_sel_hi:[1,0]
	v_pk_add_f16 v51, v51, s5 op_sel_hi:[1,0]
	v_pk_add_f16 v52, v52, s5 op_sel_hi:[1,0]
	v_pk_add_f16 v53, v53, s5 op_sel_hi:[1,0]
	v_perm_b32 v148, v240, v146, s42
	v_perm_b32 v200, v240, v147, s43
	v_pk_add_f16 v146, v148, s5 op_sel_hi:[1,0]
	v_pk_add_f16 v147, v149, s5 op_sel_hi:[1,0]
	v_pk_add_f16 v148, v198, s5 op_sel_hi:[1,0]
	v_pk_add_f16 v149, v200, s5 op_sel_hi:[1,0]
	v_cvt_pk_f16_f32 v65, v64, v65
	v_cvt_pk_f16_f32 v64, v62, v63
	v_cvt_pk_f16_f32 v62, v58, v59
	v_cvt_pk_f16_f32 v63, v60, v61
	s_waitcnt vmcnt(7)
	v_mfma_f32_32x32x16_f16 v[34:49], v[236:239], v[74:77], v[34:49]
	v_mfma_f32_32x32x16_f16 v[2:17], v[54:57], v[50:53], v[2:17]
	v_perm_b32 v58, v240, v144, s42
	v_perm_b32 v59, v240, v144, s43
	v_perm_b32 v60, v240, v145, s42
	v_perm_b32 v61, v240, v145, s43
	v_mfma_f32_32x32x16_f16 v[18:33], v[54:57], v[146:149], v[18:33]
	v_pk_add_f16 v58, v58, s5 op_sel_hi:[1,0]
	v_pk_add_f16 v59, v59, s5 op_sel_hi:[1,0]
	v_pk_add_f16 v60, v60, s5 op_sel_hi:[1,0]
	v_pk_add_f16 v61, v61, s5 op_sel_hi:[1,0]
	v_perm_b32 v144, v240, v154, s42
	v_perm_b32 v145, v240, v154, s43
	v_perm_b32 v154, v240, v155, s42
	v_perm_b32 v155, v240, v155, s43
	v_pk_add_f16 v224, v144, s5 op_sel_hi:[1,0]
	v_pk_add_f16 v225, v145, s5 op_sel_hi:[1,0]
	v_pk_add_f16 v226, v154, s5 op_sel_hi:[1,0]
	v_pk_add_f16 v227, v155, s5 op_sel_hi:[1,0]
	v_cvt_pk_f16_f32 v41, v40, v41
	v_cvt_pk_f16_f32 v40, v38, v39
	v_cvt_pk_f16_f32 v39, v36, v37
	v_cvt_pk_f16_f32 v38, v34, v35
	s_waitcnt vmcnt(6)
	v_mfma_f32_32x32x16_f16 v[2:17], v[62:65], v[58:61], v[2:17]
	v_perm_b32 v34, v240, v142, s42
	v_perm_b32 v35, v240, v142, s43
	v_mfma_f32_32x32x16_f16 v[18:33], v[62:65], v[224:227], v[18:33]
	v_perm_b32 v36, v240, v143, s42
	v_perm_b32 v37, v240, v143, s43
	v_pk_add_f16 v34, v34, s5 op_sel_hi:[1,0]
	v_pk_add_f16 v35, v35, s5 op_sel_hi:[1,0]
	v_pk_add_f16 v36, v36, s5 op_sel_hi:[1,0]
	v_pk_add_f16 v37, v37, s5 op_sel_hi:[1,0]
	v_perm_b32 v142, v240, v152, s42
	v_perm_b32 v143, v240, v152, s43
	v_perm_b32 v144, v240, v153, s42
	v_perm_b32 v53, v240, v153, s43
	v_pk_add_f16 v50, v142, s5 op_sel_hi:[1,0]
	v_pk_add_f16 v51, v143, s5 op_sel_hi:[1,0]
	v_pk_add_f16 v52, v144, s5 op_sel_hi:[1,0]
	v_pk_add_f16 v53, v53, s5 op_sel_hi:[1,0]
	v_cvt_pk_f16_f32 v49, v48, v49
	v_cvt_pk_f16_f32 v48, v46, v47
	v_cvt_pk_f16_f32 v47, v44, v45
	v_cvt_pk_f16_f32 v46, v42, v43
	v_mfma_f32_32x32x16_f16 v[2:17], v[38:41], v[34:37], v[2:17]
	s_waitcnt vmcnt(5)
	v_mfma_f32_32x32x16_f16 v[18:33], v[38:41], v[50:53], v[18:33]
	v_perm_b32 v42, v240, v140, s42
	v_perm_b32 v43, v240, v140, s43
	v_perm_b32 v44, v240, v141, s42
	v_perm_b32 v45, v240, v141, s43
	v_perm_b32 v34, v240, v150, s42
	v_perm_b32 v35, v240, v150, s43
	v_perm_b32 v36, v240, v151, s42
	v_perm_b32 v37, v240, v151, s43
	v_pk_add_f16 v42, v42, s5 op_sel_hi:[1,0]
	v_pk_add_f16 v43, v43, s5 op_sel_hi:[1,0]
	v_pk_add_f16 v44, v44, s5 op_sel_hi:[1,0]
	v_pk_add_f16 v45, v45, s5 op_sel_hi:[1,0]
	v_pk_add_f16 v34, v34, s5 op_sel_hi:[1,0]
	v_pk_add_f16 v35, v35, s5 op_sel_hi:[1,0]
	v_pk_add_f16 v36, v36, s5 op_sel_hi:[1,0]
	v_pk_add_f16 v37, v37, s5 op_sel_hi:[1,0]
	v_mfma_f32_32x32x16_f16 v[2:17], v[46:49], v[42:45], v[2:17]
	global_load_dwordx2 v[142:143], v0, s[0:1] offset:2560
	global_load_dwordx2 v[140:141], v0, s[0:1] offset:3072
	global_load_dwordx2 v[64:65], v0, s[0:1] offset:3584
	v_mfma_f32_32x32x16_f16 v[18:33], v[46:49], v[34:37], v[18:33]
	s_nop 7
	s_nop 4
	v_cvt_pk_f16_f32 v254, v2, v3
	v_cvt_pk_f16_f32 v255, v4, v5
	ds_write_b64 v251, v[254:255] offset:0
	v_pk_add_f32 v[222:223], v[222:223], v[2:3]
	v_pk_fma_f32 v[194:195], v[2:3], v[2:3], v[194:195]
	v_pk_add_f32 v[220:221], v[220:221], v[4:5]
	v_pk_fma_f32 v[192:193], v[4:5], v[4:5], v[192:193]
	v_cvt_pk_f16_f32 v252, v6, v7
	v_cvt_pk_f16_f32 v253, v8, v9
	ds_write_b64 v251, v[252:253] offset:16
	v_pk_add_f32 v[218:219], v[218:219], v[6:7]
	v_pk_fma_f32 v[184:185], v[6:7], v[6:7], v[184:185]
	v_pk_add_f32 v[216:217], v[216:217], v[8:9]
	v_pk_fma_f32 v[166:167], v[8:9], v[8:9], v[166:167]
	v_cvt_pk_f16_f32 v254, v10, v11
	v_cvt_pk_f16_f32 v255, v12, v13
	ds_write_b64 v251, v[254:255] offset:32
	v_pk_add_f32 v[214:215], v[214:215], v[10:11]
	v_pk_fma_f32 v[164:165], v[10:11], v[10:11], v[164:165]
	v_pk_add_f32 v[204:205], v[204:205], v[12:13]
	v_pk_fma_f32 v[162:163], v[12:13], v[12:13], v[162:163]
	v_cvt_pk_f16_f32 v252, v14, v15
	v_cvt_pk_f16_f32 v253, v16, v17
	ds_write_b64 v251, v[252:253] offset:48
	v_pk_add_f32 v[202:203], v[202:203], v[14:15]
	v_pk_fma_f32 v[160:161], v[14:15], v[14:15], v[160:161]
	v_pk_add_f32 v[196:197], v[196:197], v[16:17]
	v_pk_fma_f32 v[156:157], v[16:17], v[16:17], v[156:157]
	v_cvt_pk_f16_f32 v254, v18, v19
	v_cvt_pk_f16_f32 v255, v20, v21
	ds_write_b64 v251, v[254:255] offset:4608
	v_pk_add_f32 v[222:223], v[222:223], v[18:19]
	v_pk_fma_f32 v[194:195], v[18:19], v[18:19], v[194:195]
	v_pk_add_f32 v[220:221], v[220:221], v[20:21]
	v_pk_fma_f32 v[192:193], v[20:21], v[20:21], v[192:193]
	v_cvt_pk_f16_f32 v252, v22, v23
	v_cvt_pk_f16_f32 v253, v24, v25
	ds_write_b64 v251, v[252:253] offset:4624
	v_pk_add_f32 v[218:219], v[218:219], v[22:23]
	v_pk_fma_f32 v[184:185], v[22:23], v[22:23], v[184:185]
	v_pk_add_f32 v[216:217], v[216:217], v[24:25]
	v_pk_fma_f32 v[166:167], v[24:25], v[24:25], v[166:167]
	v_cvt_pk_f16_f32 v254, v26, v27
	v_cvt_pk_f16_f32 v255, v28, v29
	ds_write_b64 v251, v[254:255] offset:4640
	v_pk_add_f32 v[214:215], v[214:215], v[26:27]
	v_pk_fma_f32 v[164:165], v[26:27], v[26:27], v[164:165]
	v_pk_add_f32 v[204:205], v[204:205], v[28:29]
	v_pk_fma_f32 v[162:163], v[28:29], v[28:29], v[162:163]
	v_cvt_pk_f16_f32 v252, v30, v31
	v_cvt_pk_f16_f32 v253, v32, v33
	ds_write_b64 v251, v[252:253] offset:4656
	v_pk_add_f32 v[202:203], v[202:203], v[30:31]
	v_pk_fma_f32 v[160:161], v[30:31], v[30:31], v[160:161]
	v_pk_add_f32 v[196:197], v[196:197], v[32:33]
	v_pk_fma_f32 v[156:157], v[32:33], v[32:33], v[156:157]
	s_nop 7
	s_waitcnt lgkmcnt(0)
	s_barrier
	s_nop 1
	ds_read_b128 v[16:19], v159 offset:43520
	s_waitcnt lgkmcnt(0)
	v_mfma_f32_32x32x16_f16 v[32:47], v[16:19], v[126:129], 0
	ds_read_b128 v[2:5], v159 offset:34816
	s_waitcnt lgkmcnt(0)
	v_mfma_f32_32x32x16_f16 v[48:63], v[2:5], v[126:129], 0
	ds_read_b128 v[126:129], v159 offset:34848
	s_waitcnt lgkmcnt(0)
	v_mfma_f32_32x32x16_f16 v[48:63], v[126:129], v[118:121], v[48:63]
	v_mfma_f32_32x32x16_f16 v[0:15], v[122:125], v[2:5], v[168:183]
	v_mfma_f32_32x32x16_f16 v[0:15], v[114:117], v[126:129], v[0:15]
	v_mfma_f32_32x32x16_f16 v[16:31], v[122:125], v[16:19], v[168:183]
	ds_read_b128 v[122:125], v159 offset:43552
	s_waitcnt lgkmcnt(0)
	v_mfma_f32_32x32x16_f16 v[32:47], v[122:125], v[118:121], v[32:47]
	v_mfma_f32_32x32x16_f16 v[16:31], v[114:117], v[122:125], v[16:31]
	ds_read_b128 v[118:121], v159 offset:34880
	ds_read_b128 v[114:117], v159 offset:43584
	s_waitcnt lgkmcnt(1)
	v_mfma_f32_32x32x16_f16 v[48:63], v[118:121], v[110:113], v[48:63]
	s_waitcnt lgkmcnt(0)
	v_mfma_f32_32x32x16_f16 v[32:47], v[114:117], v[110:113], v[32:47]
	v_mfma_f32_32x32x16_f16 v[0:15], v[106:109], v[118:121], v[0:15]
	ds_read_b128 v[110:113], v159 offset:34912
	v_mfma_f32_32x32x16_f16 v[16:31], v[106:109], v[114:117], v[16:31]
	ds_read_b128 v[106:109], v159 offset:43616
	s_waitcnt lgkmcnt(1)
	v_mfma_f32_32x32x16_f16 v[48:63], v[110:113], v[102:105], v[48:63]
	s_waitcnt lgkmcnt(0)
	v_mfma_f32_32x32x16_f16 v[32:47], v[106:109], v[102:105], v[32:47]
	v_mfma_f32_32x32x16_f16 v[0:15], v[98:101], v[110:113], v[0:15]
	ds_read_b128 v[102:105], v159 offset:34944
	v_mfma_f32_32x32x16_f16 v[16:31], v[98:101], v[106:109], v[16:31]
	ds_read_b128 v[98:101], v159 offset:43648
	s_waitcnt lgkmcnt(1)
	v_mfma_f32_32x32x16_f16 v[48:63], v[102:105], v[94:97], v[48:63]
	s_waitcnt lgkmcnt(0)
	v_mfma_f32_32x32x16_f16 v[32:47], v[98:101], v[94:97], v[32:47]
	v_mfma_f32_32x32x16_f16 v[0:15], v[86:89], v[102:105], v[0:15]
	ds_read_b128 v[94:97], v159 offset:34976
	v_mfma_f32_32x32x16_f16 v[16:31], v[86:89], v[98:101], v[16:31]
	ds_read_b128 v[86:89], v159 offset:43680
	s_waitcnt lgkmcnt(1)
	v_mfma_f32_32x32x16_f16 v[48:63], v[94:97], v[90:93], v[48:63]
	s_waitcnt lgkmcnt(0)
	v_mfma_f32_32x32x16_f16 v[32:47], v[86:89], v[90:93], v[32:47]
	v_mfma_f32_32x32x16_f16 v[0:15], v[78:81], v[94:97], v[0:15]
	ds_read_b128 v[90:93], v159 offset:35008
	v_mfma_f32_32x32x16_f16 v[16:31], v[78:81], v[86:89], v[16:31]
	ds_read_b128 v[78:81], v159 offset:43712
	s_waitcnt lgkmcnt(1)
	v_mfma_f32_32x32x16_f16 v[48:63], v[90:93], v[82:85], v[48:63]
	s_waitcnt lgkmcnt(0)
	v_mfma_f32_32x32x16_f16 v[32:47], v[78:81], v[82:85], v[32:47]
	v_mfma_f32_32x32x16_f16 v[0:15], v[70:73], v[90:93], v[0:15]
	ds_read_b128 v[82:85], v159 offset:35040
	v_mfma_f32_32x32x16_f16 v[16:31], v[70:73], v[78:81], v[16:31]
	ds_read_b128 v[70:73], v159 offset:43744
	s_waitcnt lgkmcnt(1)
	v_mfma_f32_32x32x16_f16 v[48:63], v[82:85], v[74:77], v[48:63]
	v_mfma_f32_32x32x16_f16 v[0:15], v[66:69], v[82:85], v[0:15]
	s_nop 3
	s_nop 6
	v_cvt_pk_f16_f32 v55, v54, v55
	v_cvt_pk_f16_f32 v54, v52, v53
	v_cvt_pk_f16_f32 v53, v50, v51
	v_cvt_pk_f16_f32 v52, v48, v49
	s_waitcnt vmcnt(3)
	s_waitcnt lgkmcnt(0)
	v_mfma_f32_32x32x16_f16 v[16:31], v[66:69], v[70:73], v[16:31]
	v_lshrrev_b32_e32 v69, 16, v139
	v_mfma_f32_32x32x16_f16 v[32:47], v[70:73], v[74:77], v[32:47]
	v_lshrrev_b32_e32 v70, 8, v139
	v_perm_b32 v69, v70, v69, s4
	v_perm_b32 v66, v240, v138, s42
	v_perm_b32 v67, v240, v138, s43
	v_perm_b32 v68, v240, v139, s42
	v_or_b32_e32 v69, 0x64006400, v69
	v_pk_add_f16 v66, v66, s5 op_sel_hi:[1,0]
	v_pk_add_f16 v67, v67, s5 op_sel_hi:[1,0]
	v_pk_add_f16 v68, v68, s5 op_sel_hi:[1,0]
	v_pk_add_f16 v69, v69, s5 op_sel_hi:[1,0]
	s_nop 1
	v_mfma_f32_32x32x16_f16 v[0:15], v[52:55], v[66:69], v[0:15]
	v_perm_b32 v48, v240, v136, s42
	v_perm_b32 v49, v240, v136, s43
	v_perm_b32 v50, v240, v137, s42
	v_perm_b32 v51, v240, v137, s43
	v_pk_add_f16 v48, v48, s5 op_sel_hi:[1,0]
	v_pk_add_f16 v49, v49, s5 op_sel_hi:[1,0]
	v_pk_add_f16 v50, v50, s5 op_sel_hi:[1,0]
	v_pk_add_f16 v51, v51, s5 op_sel_hi:[1,0]
	v_cvt_pk_f16_f32 v39, v38, v39
	v_cvt_pk_f16_f32 v38, v36, v37
	v_mfma_f32_32x32x16_f16 v[16:31], v[52:55], v[48:51], v[16:31]
	v_perm_b32 v48, v240, v134, s42
	v_perm_b32 v49, v240, v134, s43
	v_perm_b32 v50, v240, v135, s42
	v_perm_b32 v51, v240, v135, s43
	v_pk_add_f16 v48, v48, s5 op_sel_hi:[1,0]
	v_pk_add_f16 v49, v49, s5 op_sel_hi:[1,0]
	v_pk_add_f16 v50, v50, s5 op_sel_hi:[1,0]
	v_pk_add_f16 v51, v51, s5 op_sel_hi:[1,0]
	v_cvt_pk_f16_f32 v55, v62, v63
	v_cvt_pk_f16_f32 v54, v60, v61
	v_cvt_pk_f16_f32 v53, v58, v59
	v_cvt_pk_f16_f32 v52, v56, v57
	s_waitcnt vmcnt(2)
	v_cvt_pk_f16_f32 v37, v34, v35
	v_mfma_f32_32x32x16_f16 v[0:15], v[52:55], v[48:51], v[0:15]
	v_perm_b32 v48, v240, v142, s42
	v_perm_b32 v49, v240, v142, s43
	v_perm_b32 v50, v240, v143, s42
	v_perm_b32 v51, v240, v143, s43
	v_pk_add_f16 v48, v48, s5 op_sel_hi:[1,0]
	v_pk_add_f16 v49, v49, s5 op_sel_hi:[1,0]
	v_pk_add_f16 v50, v50, s5 op_sel_hi:[1,0]
	v_pk_add_f16 v51, v51, s5 op_sel_hi:[1,0]
	v_cvt_pk_f16_f32 v36, v32, v33
	s_waitcnt vmcnt(1)
	v_mfma_f32_32x32x16_f16 v[16:31], v[52:55], v[48:51], v[16:31]
	v_lshrrev_b32_e32 v51, 16, v133
	v_lshrrev_b32_e32 v52, 8, v133
	v_perm_b32 v51, v52, v51, s4
	v_perm_b32 v48, v240, v132, s42
	v_perm_b32 v49, v240, v132, s43
	v_perm_b32 v50, v240, v133, s42
	v_or_b32_e32 v51, 0x64006400, v51
	v_pk_add_f16 v48, v48, s5 op_sel_hi:[1,0]
	v_pk_add_f16 v49, v49, s5 op_sel_hi:[1,0]
	v_pk_add_f16 v50, v50, s5 op_sel_hi:[1,0]
	v_pk_add_f16 v51, v51, s5 op_sel_hi:[1,0]
	s_nop 1
	v_mfma_f32_32x32x16_f16 v[0:15], v[36:39], v[48:51], v[0:15]
	v_perm_b32 v32, v240, v140, s42
	v_perm_b32 v33, v240, v140, s43
	v_perm_b32 v34, v240, v141, s42
	v_perm_b32 v35, v240, v141, s43
	v_pk_add_f16 v32, v32, s5 op_sel_hi:[1,0]
	v_pk_add_f16 v33, v33, s5 op_sel_hi:[1,0]
	v_pk_add_f16 v34, v34, s5 op_sel_hi:[1,0]
	v_pk_add_f16 v35, v35, s5 op_sel_hi:[1,0]
	s_nop 1
	v_mfma_f32_32x32x16_f16 v[16:31], v[36:39], v[32:35], v[16:31]
	v_perm_b32 v32, v240, v130, s42
	v_perm_b32 v33, v240, v130, s43
	v_perm_b32 v34, v240, v131, s42
	v_perm_b32 v35, v240, v131, s43
	v_pk_add_f16 v32, v32, s5 op_sel_hi:[1,0]
	v_pk_add_f16 v33, v33, s5 op_sel_hi:[1,0]
	v_pk_add_f16 v34, v34, s5 op_sel_hi:[1,0]
	v_pk_add_f16 v35, v35, s5 op_sel_hi:[1,0]
	v_cvt_pk_f16_f32 v39, v46, v47
	v_cvt_pk_f16_f32 v38, v44, v45
	v_cvt_pk_f16_f32 v37, v42, v43
	v_cvt_pk_f16_f32 v36, v40, v41
	s_waitcnt vmcnt(0)
	s_nop 0
	v_mfma_f32_32x32x16_f16 v[0:15], v[36:39], v[32:35], v[0:15]
	v_perm_b32 v32, v240, v64, s42
	v_perm_b32 v33, v240, v64, s43
	v_perm_b32 v34, v240, v65, s42
	v_perm_b32 v35, v240, v65, s43
	v_pk_add_f16 v32, v32, s5 op_sel_hi:[1,0]
	v_pk_add_f16 v33, v33, s5 op_sel_hi:[1,0]
	v_pk_add_f16 v34, v34, s5 op_sel_hi:[1,0]
	v_pk_add_f16 v35, v35, s5 op_sel_hi:[1,0]
	s_nop 3
	v_mfma_f32_32x32x16_f16 v[16:31], v[36:39], v[32:35], v[16:31]
	s_nop 7
	s_nop 4
	v_cvt_pk_f16_f32 v254, v0, v1
	v_cvt_pk_f16_f32 v255, v2, v3
	ds_write_b64 v251, v[254:255] offset:18432
	v_pk_add_f32 v[222:223], v[222:223], v[0:1]
	v_pk_fma_f32 v[194:195], v[0:1], v[0:1], v[194:195]
	v_pk_add_f32 v[220:221], v[220:221], v[2:3]
	v_pk_fma_f32 v[192:193], v[2:3], v[2:3], v[192:193]
	v_cvt_pk_f16_f32 v252, v4, v5
	v_cvt_pk_f16_f32 v253, v6, v7
	ds_write_b64 v251, v[252:253] offset:18448
	v_pk_add_f32 v[218:219], v[218:219], v[4:5]
	v_pk_fma_f32 v[184:185], v[4:5], v[4:5], v[184:185]
	v_pk_add_f32 v[216:217], v[216:217], v[6:7]
	v_pk_fma_f32 v[166:167], v[6:7], v[6:7], v[166:167]
	v_cvt_pk_f16_f32 v254, v8, v9
	v_cvt_pk_f16_f32 v255, v10, v11
	ds_write_b64 v251, v[254:255] offset:18464
	v_pk_add_f32 v[214:215], v[214:215], v[8:9]
	v_pk_fma_f32 v[164:165], v[8:9], v[8:9], v[164:165]
	v_pk_add_f32 v[204:205], v[204:205], v[10:11]
	v_pk_fma_f32 v[162:163], v[10:11], v[10:11], v[162:163]
	v_cvt_pk_f16_f32 v252, v12, v13
	v_cvt_pk_f16_f32 v253, v14, v15
	ds_write_b64 v251, v[252:253] offset:18480
	v_pk_add_f32 v[202:203], v[202:203], v[12:13]
	v_pk_fma_f32 v[160:161], v[12:13], v[12:13], v[160:161]
	v_pk_add_f32 v[196:197], v[196:197], v[14:15]
	v_pk_fma_f32 v[156:157], v[14:15], v[14:15], v[156:157]
	v_cvt_pk_f16_f32 v254, v16, v17
	v_cvt_pk_f16_f32 v255, v18, v19
	ds_write_b64 v251, v[254:255] offset:23040
	v_pk_add_f32 v[222:223], v[222:223], v[16:17]
	v_pk_fma_f32 v[194:195], v[16:17], v[16:17], v[194:195]
	v_pk_add_f32 v[220:221], v[220:221], v[18:19]
	v_pk_fma_f32 v[192:193], v[18:19], v[18:19], v[192:193]
	v_cvt_pk_f16_f32 v252, v20, v21
	v_cvt_pk_f16_f32 v253, v22, v23
	ds_write_b64 v251, v[252:253] offset:23056
	v_pk_add_f32 v[218:219], v[218:219], v[20:21]
	v_pk_fma_f32 v[184:185], v[20:21], v[20:21], v[184:185]
	v_pk_add_f32 v[216:217], v[216:217], v[22:23]
	v_pk_fma_f32 v[166:167], v[22:23], v[22:23], v[166:167]
	v_cvt_pk_f16_f32 v254, v24, v25
	v_cvt_pk_f16_f32 v255, v26, v27
	ds_write_b64 v251, v[254:255] offset:23072
	v_pk_add_f32 v[214:215], v[214:215], v[24:25]
	v_pk_fma_f32 v[164:165], v[24:25], v[24:25], v[164:165]
	v_pk_add_f32 v[204:205], v[204:205], v[26:27]
	v_pk_fma_f32 v[162:163], v[26:27], v[26:27], v[162:163]
	v_cvt_pk_f16_f32 v252, v28, v29
	v_cvt_pk_f16_f32 v253, v30, v31
	ds_write_b64 v251, v[252:253] offset:23088
	v_pk_add_f32 v[202:203], v[202:203], v[28:29]
	v_pk_fma_f32 v[160:161], v[28:29], v[28:29], v[160:161]
	v_pk_add_f32 v[196:197], v[196:197], v[30:31]
	v_pk_fma_f32 v[156:157], v[30:31], v[30:31], v[156:157]
	s_nop 4
	s_nop 0
	v_add_f32_dpp v222, v222, v222 row_half_mirror row_mask:0xf bank_mask:0x5
	v_add_f32_dpp v222, v223, v223 row_half_mirror row_mask:0xf bank_mask:0xa
	v_add_f32_dpp v220, v220, v220 row_half_mirror row_mask:0xf bank_mask:0x5
	v_add_f32_dpp v220, v221, v221 row_half_mirror row_mask:0xf bank_mask:0xa
	v_add_f32_dpp v218, v218, v218 row_half_mirror row_mask:0xf bank_mask:0x5
	v_add_f32_dpp v218, v219, v219 row_half_mirror row_mask:0xf bank_mask:0xa
	v_add_f32_dpp v216, v216, v216 row_half_mirror row_mask:0xf bank_mask:0x5
	v_add_f32_dpp v216, v217, v217 row_half_mirror row_mask:0xf bank_mask:0xa
	v_add_f32_dpp v214, v214, v214 row_half_mirror row_mask:0xf bank_mask:0x5
	v_add_f32_dpp v214, v215, v215 row_half_mirror row_mask:0xf bank_mask:0xa
	v_add_f32_dpp v204, v204, v204 row_half_mirror row_mask:0xf bank_mask:0x5
	v_add_f32_dpp v204, v205, v205 row_half_mirror row_mask:0xf bank_mask:0xa
	v_add_f32_dpp v202, v202, v202 row_half_mirror row_mask:0xf bank_mask:0x5
	v_add_f32_dpp v202, v203, v203 row_half_mirror row_mask:0xf bank_mask:0xa
	v_add_f32_dpp v196, v196, v196 row_half_mirror row_mask:0xf bank_mask:0x5
	v_add_f32_dpp v196, v197, v197 row_half_mirror row_mask:0xf bank_mask:0xa
	v_add_f32_dpp v194, v194, v194 row_half_mirror row_mask:0xf bank_mask:0x5
	v_add_f32_dpp v194, v195, v195 row_half_mirror row_mask:0xf bank_mask:0xa
	v_add_f32_dpp v192, v192, v192 row_half_mirror row_mask:0xf bank_mask:0x5
	v_add_f32_dpp v192, v193, v193 row_half_mirror row_mask:0xf bank_mask:0xa
	v_add_f32_dpp v184, v184, v184 row_half_mirror row_mask:0xf bank_mask:0x5
	v_add_f32_dpp v184, v185, v185 row_half_mirror row_mask:0xf bank_mask:0xa
	v_add_f32_dpp v166, v166, v166 row_half_mirror row_mask:0xf bank_mask:0x5
	v_add_f32_dpp v166, v167, v167 row_half_mirror row_mask:0xf bank_mask:0xa
	v_add_f32_dpp v164, v164, v164 row_half_mirror row_mask:0xf bank_mask:0x5
	v_add_f32_dpp v164, v165, v165 row_half_mirror row_mask:0xf bank_mask:0xa
	v_add_f32_dpp v162, v162, v162 row_half_mirror row_mask:0xf bank_mask:0x5
	v_add_f32_dpp v162, v163, v163 row_half_mirror row_mask:0xf bank_mask:0xa
	v_add_f32_dpp v160, v160, v160 row_half_mirror row_mask:0xf bank_mask:0x5
	v_add_f32_dpp v160, v161, v161 row_half_mirror row_mask:0xf bank_mask:0xa
	v_add_f32_dpp v156, v156, v156 row_half_mirror row_mask:0xf bank_mask:0x5
	v_add_f32_dpp v156, v157, v157 row_half_mirror row_mask:0xf bank_mask:0xa
	v_add_f32_dpp v222, v222, v222 row_ror:8 row_mask:0xf bank_mask:0x3
	v_add_f32_dpp v222, v220, v220 row_ror:8 row_mask:0xf bank_mask:0xc
	v_add_f32_dpp v218, v218, v218 row_ror:8 row_mask:0xf bank_mask:0x3
	v_add_f32_dpp v218, v216, v216 row_ror:8 row_mask:0xf bank_mask:0xc
	v_add_f32_dpp v214, v214, v214 row_ror:8 row_mask:0xf bank_mask:0x3
	v_add_f32_dpp v214, v204, v204 row_ror:8 row_mask:0xf bank_mask:0xc
	v_add_f32_dpp v202, v202, v202 row_ror:8 row_mask:0xf bank_mask:0x3
	v_add_f32_dpp v202, v196, v196 row_ror:8 row_mask:0xf bank_mask:0xc
	v_add_f32_dpp v194, v194, v194 row_ror:8 row_mask:0xf bank_mask:0x3
	v_add_f32_dpp v194, v192, v192 row_ror:8 row_mask:0xf bank_mask:0xc
	v_add_f32_dpp v184, v184, v184 row_ror:8 row_mask:0xf bank_mask:0x3
	v_add_f32_dpp v184, v166, v166 row_ror:8 row_mask:0xf bank_mask:0xc
	v_add_f32_dpp v164, v164, v164 row_ror:8 row_mask:0xf bank_mask:0x3
	v_add_f32_dpp v164, v162, v162 row_ror:8 row_mask:0xf bank_mask:0xc
	v_add_f32_dpp v160, v160, v160 row_ror:8 row_mask:0xf bank_mask:0x3
	v_add_f32_dpp v160, v156, v156 row_ror:8 row_mask:0xf bank_mask:0xc
	v_add_f32_dpp v222, v222, v222 quad_perm:[1,0,3,2] row_mask:0xf bank_mask:0xf
	v_add_f32_dpp v218, v218, v218 quad_perm:[1,0,3,2] row_mask:0xf bank_mask:0xf
	v_add_f32_dpp v214, v214, v214 quad_perm:[1,0,3,2] row_mask:0xf bank_mask:0xf
	v_add_f32_dpp v202, v202, v202 quad_perm:[1,0,3,2] row_mask:0xf bank_mask:0xf
	v_add_f32_dpp v194, v194, v194 quad_perm:[1,0,3,2] row_mask:0xf bank_mask:0xf
	v_add_f32_dpp v184, v184, v184 quad_perm:[1,0,3,2] row_mask:0xf bank_mask:0xf
	v_add_f32_dpp v164, v164, v164 quad_perm:[1,0,3,2] row_mask:0xf bank_mask:0xf
	v_add_f32_dpp v160, v160, v160 quad_perm:[1,0,3,2] row_mask:0xf bank_mask:0xf
	v_add_f32_dpp v222, v222, v222 quad_perm:[2,3,0,1] row_mask:0xf bank_mask:0xf
	v_add_f32_dpp v218, v218, v218 quad_perm:[2,3,0,1] row_mask:0xf bank_mask:0xf
	v_add_f32_dpp v214, v214, v214 quad_perm:[2,3,0,1] row_mask:0xf bank_mask:0xf
	v_add_f32_dpp v202, v202, v202 quad_perm:[2,3,0,1] row_mask:0xf bank_mask:0xf
	v_add_f32_dpp v194, v194, v194 quad_perm:[2,3,0,1] row_mask:0xf bank_mask:0xf
	v_add_f32_dpp v184, v184, v184 quad_perm:[2,3,0,1] row_mask:0xf bank_mask:0xf
	v_add_f32_dpp v164, v164, v164 quad_perm:[2,3,0,1] row_mask:0xf bank_mask:0xf
	v_add_f32_dpp v160, v160, v160 quad_perm:[2,3,0,1] row_mask:0xf bank_mask:0xf
	s_mov_b32 exec_lo, 0x11111111
	s_mov_b32 exec_hi, 0x11111111
	ds_add_f32 v250, v222 offset:0
	ds_add_f32 v250, v218 offset:32
	ds_add_f32 v250, v214 offset:64
	ds_add_f32 v250, v202 offset:96
	ds_add_f32 v250, v194 offset:256
	ds_add_f32 v250, v184 offset:288
	ds_add_f32 v250, v164 offset:320
	ds_add_f32 v250, v160 offset:352
	s_mov_b64 exec, -1
	s_waitcnt lgkmcnt(0)
	s_barrier
	s_cmp_lg_u32 s50, 0
	s_cbranch_scc1 .LBB2_27
	v_mbcnt_lo_u32_b32 v2, -1, 0
	v_mbcnt_hi_u32_b32 v2, -1, v2
	v_and_b32_e32 v3, 32, v2
	v_add_u32_e32 v4, v2, v3
	v_lshl_add_u32 v5, v4, 2, s49
	ds_read_b32 v6, v5
	v_lshl_add_u32 v4, v3, 1, v4
	v_add_u32_e32 v4, s48, v4
	v_lshlrev_b32_e32 v4, 2, v4
	s_waitcnt lgkmcnt(0)
	global_atomic_add_f32 v4, v6, s[46:47]

.LBB3_10:
	v_mov_b32_e32 v11, v0
	s_waitcnt lgkmcnt(0)
	s_barrier
	s_lshl_b32 s8, s19, 7
	s_waitcnt vmcnt(7)
	v_add_u32_e32 v2, 0xffffff00, v11
	v_lshlrev_b32_e32 v3, 3, v11
	v_and_b32_e32 v3, 56, v3
	v_mov_b32_e32 v4, 0x11000
	v_lshrrev_b32_e32 v12, 3, v2
	v_ashrrev_i32_e32 v2, 3, v2
	s_movk_i32 s10, 0xffc0
	s_or_b32 s8, s8, s18
	v_lshl_or_b32 v10, v3, 1, v4
	v_bfi_b32 v7, s10, v2, v12
	s_movk_i32 s11, 0x90
	v_or_b32_e32 v6, s8, v3
	v_mad_u64_u32 v[2:3], s[8:9], v7, s11, v[10:11]
	ds_read_b128 v[2:5], v2 offset:18432
	v_lshlrev_b32_e32 v14, 1, v6
	v_lshl_add_u32 v13, v7, 8, v14
	v_lshrrev_b32_e32 v15, 3, v11
	v_ashrrev_i32_e32 v6, 3, v11
	s_waitcnt lgkmcnt(0)
	buffer_store_dwordx4 v[2:5], v13, s[4:7], 0 offen sc1
	v_bfi_b32 v16, s10, v6, v15
	v_mad_u64_u32 v[6:7], s[8:9], v16, s11, v[10:11]
	v_add_u32_e32 v2, 0x100, v11
	v_ashrrev_i32_e32 v2, 3, v2
	v_bfi_b32 v17, s10, v2, v12
	v_mad_u64_u32 v[2:3], s[8:9], v17, s11, v[10:11]
	v_add_u32_e32 v11, 0x200, v11
	v_ashrrev_i32_e32 v11, 3, v11
	ds_read_b128 v[6:9], v6 offset:18432
	v_bfi_b32 v15, s10, v11, v15
	ds_read_b128 v[2:5], v2 offset:18432
	v_mad_u64_u32 v[10:11], s[8:9], v15, s11, v[10:11]
	ds_read_b128 v[10:13], v10 offset:18432
	v_lshl_add_u32 v16, v16, 8, v14
	s_waitcnt lgkmcnt(2)
	buffer_store_dwordx4 v[6:9], v16, s[4:7], 0 offen sc1
	s_nop 1
	v_lshl_add_u32 v6, v17, 8, v14
	s_waitcnt lgkmcnt(1)
	buffer_store_dwordx4 v[2:5], v6, s[4:7], 0 offen sc1
	s_nop 1
	v_lshl_add_u32 v2, v15, 8, v14
	s_waitcnt lgkmcnt(0)
	buffer_store_dwordx4 v[10:13], v2, s[4:7], 0 offen sc1
	s_mov_b64 s[2:3], 0
.LBB3_17:
	s_and_b64 vcc, exec, s[2:3]
	s_cbranch_vccz .LBB3_27
	s_load_dwordx2 s[46:47], s[0:1], 0x90
	s_lshr_b32 s50, s15, 7
	s_bfe_u32 s51, s15, 0x10006
	s_and_b32 s48, s12, 7
	s_lshl_b32 s48, s48, 8
	s_lshl_b32 s49, s14, 6
	s_or_b32 s48, s48, s49
	s_lshl_b32 s49, s51, 5
	s_or_b32 s48, s48, s49
	s_lshl_b32 s49, s51, 7
	s_add_i32 s49, s49, 0x1e400
	v_mov_b32_e32 v240, 0x64646464
	s_mov_b32 s42, 0x4010400
	s_mov_b32 s43, 0x4030402
	s_load_dwordx2 s[8:9], s[0:1], 0x70
	s_load_dwordx4 s[4:7], s[0:1], 0x40
	s_load_dwordx4 s[20:23], s[0:1], 0x10
	s_load_dwordx4 s[28:31], s[0:1], 0x20
	s_load_dwordx4 s[32:35], s[0:1], 0x30
	s_load_dwordx2 s[36:37], s[0:1], 0x60
	v_mov_b32_e32 v3, 0
	v_lshlrev_b32_e32 v2, 2, v0
	s_movk_i32 s2, 0xfe00
	s_mov_b32 s3, -1
	s_waitcnt lgkmcnt(0)
	v_lshl_add_u64 v[6:7], s[22:23], 0, v[2:3]
	s_lshr_b32 s16, s15, 7
	s_movk_i32 s10, 0x80
	v_lshl_add_u64 v[6:7], v[6:7], 0, s[2:3]
	s_lshl_b32 s2, s12, 3
	v_cmp_gt_u32_e32 vcc, s10, v0
	s_or_b32 s10, s16, s2
	v_lshl_add_u64 v[4:5], s[20:21], 0, v[2:3]
	s_ashr_i32 s11, s10, 31
	v_cndmask_b32_e32 v6, v6, v4, vcc
	s_movk_i32 s17, 0x1000
	s_bfe_u32 s13, s15, 0x10006
	s_lshl_b64 s[2:3], s[10:11], 12
	v_and_b32_e32 v156, 63, v0
	v_cndmask_b32_e32 v7, v7, v5, vcc
	v_add_co_u32_e32 v20, vcc, s17, v6
	s_add_u32 s2, s8, s2
	s_nop 0
	v_addc_co_u32_e32 v21, vcc, 0, v7, vcc
	s_addc_u32 s3, s9, s3
	v_lshlrev_b32_e32 v1, 3, v156
	global_load_dword v17, v[6:7], off
	global_load_dword v16, v[6:7], off offset:512
	global_load_dword v13, v[6:7], off offset:1024
	global_load_dword v12, v[6:7], off offset:1536
	global_load_dword v9, v[6:7], off offset:2048
	global_load_dword v8, v[6:7], off offset:2560
	global_load_dword v5, v[6:7], off offset:3072
	global_load_dword v4, v[6:7], off offset:3584
	global_load_dword v19, v[20:21], off
	global_load_dword v18, v[20:21], off offset:512
	global_load_dword v15, v[20:21], off offset:1024
	global_load_dword v14, v[20:21], off offset:1536
	global_load_dword v11, v[20:21], off offset:2048
	global_load_dword v10, v[20:21], off offset:2560
	global_load_dword v7, v[20:21], off offset:3072
	global_load_dword v6, v[20:21], off offset:3584
	s_cmpk_lt_u32 s15, 0x80
	s_cselect_b32 s38, s28, s32
	s_cselect_b32 s39, s29, s33
	s_cselect_b32 s40, s30, s34
	s_cselect_b32 s41, s31, s35
	v_and_b32_e32 v24, 0x1fc, v2
	v_and_b32_e32 v28, 0xfc, v2
	v_lshl_or_b32 v28, s14, 8, v28
	global_load_dword v25, v24, s[38:39]
	global_load_dword v26, v24, s[40:41]
	global_load_dword v27, v28, s[36:37]
	global_load_dwordx2 v[154:155], v1, s[2:3]
	global_load_dwordx2 v[150:151], v1, s[2:3] offset:512
	global_load_dwordx2 v[146:147], v1, s[2:3] offset:1024
	global_load_dwordx2 v[142:143], v1, s[2:3] offset:1536
	global_load_dwordx2 v[152:153], v1, s[2:3] offset:2048
	global_load_dwordx2 v[148:149], v1, s[2:3] offset:2560
	global_load_dwordx2 v[144:145], v1, s[2:3] offset:3072
	global_load_dwordx2 v[140:141], v1, s[2:3] offset:3584
	s_lshl_b32 s2, s14, 10
	s_lshl_b32 s3, s13, 9
	s_or_b32 s2, s3, s2
	v_or_b32_e32 v1, s2, v156
	v_lshlrev_b32_e32 v20, 4, v1
	v_mov_b32_e32 v21, v3
	v_lshl_add_u64 v[22:23], s[4:5], 0, v[20:21]
	v_add_co_u32_e32 v22, vcc, s17, v22
	s_movk_i32 s2, 0x7f
	s_nop 0
	v_addc_co_u32_e32 v23, vcc, 0, v23, vcc
	global_load_dwordx4 v[86:89], v[22:23], off
	global_load_dwordx4 v[78:81], v[22:23], off offset:1024
	global_load_dwordx4 v[70:73], v[22:23], off offset:2048
	global_load_dwordx4 v[66:69], v[22:23], off offset:3072
	global_load_dwordx4 v[122:125], v20, s[4:5]
	global_load_dwordx4 v[126:129], v20, s[6:7]
	global_load_dwordx4 v[114:117], v20, s[4:5] offset:1024
	global_load_dwordx4 v[118:121], v20, s[6:7] offset:1024
	global_load_dwordx4 v[106:109], v20, s[4:5] offset:2048
	global_load_dwordx4 v[110:113], v20, s[6:7] offset:2048
	global_load_dwordx4 v[98:101], v20, s[4:5] offset:3072
	global_load_dwordx4 v[102:105], v20, s[6:7] offset:3072
	v_lshl_add_u64 v[22:23], s[6:7], 0, v[20:21]
	v_add_co_u32_e32 v20, vcc, 0x1000, v22
	s_nop 1
	v_addc_co_u32_e32 v21, vcc, 0, v23, vcc
	global_load_dwordx4 v[94:97], v[20:21], off
	global_load_dwordx4 v[90:93], v[20:21], off offset:1024
	global_load_dwordx4 v[82:85], v[20:21], off offset:2048
	global_load_dwordx4 v[74:77], v[20:21], off offset:3072
	v_cmp_lt_u32_e32 vcc, s2, v0
	v_cmp_gt_u32_e64 s[2:3], 64, v0
	s_and_saveexec_b64 s[4:5], s[2:3]
	s_cbranch_execz .LBB3_20
	v_add_u32_e32 v20, 0x1ee00, v2
	s_waitcnt vmcnt(24)
	ds_write_b32 v20, v27

.LBB3_24:
	s_or_b64 exec, exec, s[2:3]
	v_and_b32_e32 v1, 31, v0
	v_lshlrev_b32_e32 v2, 2, v1
	v_lshl_or_b32 v2, s13, 7, v2
	v_or_b32_e32 v2, 0x1ee00, v2
	v_lshrrev_b32_e32 v158, 5, v156
	s_waitcnt lgkmcnt(0)
	s_barrier
	v_lshlrev_b32_e32 v250, 4, v158
	v_lshl_or_b32 v250, s13, 7, v250
	v_or_b32_e32 v254, 0x1ee00, v250
	ds_read_b128 v[168:171], v254 offset:0
	ds_read_b128 v[172:175], v254 offset:32
	ds_read_b128 v[176:179], v254 offset:64
	ds_read_b128 v[180:183], v254 offset:96
	v_bfe_u32 v255, v156, 2, 2
	v_lshl_add_u32 v250, v255, 2, v250
	v_add_u32_e32 v250, 0x1e400, v250
	s_waitcnt lgkmcnt(0)
	s_barrier
	ds_read_b32 v157, v2
	v_mul_u32_u24_e32 v2, 0x88, v1
	s_mul_i32 s0, s16, 0x4400
	v_lshlrev_b32_e32 v2, 1, v2
	v_lshlrev_b32_e32 v3, 4, v158
	v_mov_b32_e32 v138, v0
	v_add3_u32 v159, s0, v2, v3
	ds_read_b128 v[2:5], v159
	ds_read_b128 v[18:21], v159 offset:8704
	ds_read_b128 v[130:133], v159 offset:32
	s_waitcnt vmcnt(10) lgkmcnt(2)
	v_mfma_f32_32x32x16_f16 v[50:65], v[2:5], v[126:129], 0
	s_mov_b32 s2, 0xc060c00
	s_mov_b32 s3, 0xe400
	s_mulk_i32 s16, 0x2400
	s_lshl_b32 s0, s13, 6
	s_or_b32 s0, s16, s0
	s_add_i32 s0, s0, 0x11000
	v_mul_u32_u24_e32 v251, 0x90, v1
	v_lshl_add_u32 v251, v158, 3, v251
	v_add_u32_e32 v251, s0, v251
	s_waitcnt lgkmcnt(1)
	v_mfma_f32_32x32x16_f16 v[34:49], v[18:21], v[126:129], 0
	s_or_b32 s0, s10, 2
	s_ashr_i32 s1, s0, 31
	s_lshl_b64 s[0:1], s[0:1], 12
	s_add_u32 s0, s8, s0
	s_addc_u32 s1, s9, s1
	v_cmp_gt_u32_e32 vcc, 32, v156
	v_mfma_f32_32x32x16_f16 v[2:17], v[122:125], v[2:5], v[168:183]
	v_mfma_f32_32x32x16_f16 v[18:33], v[122:125], v[18:21], v[168:183]
	ds_read_b128 v[134:137], v159 offset:8736
	ds_read_b128 v[160:163], v159 offset:64
	s_waitcnt vmcnt(8) lgkmcnt(2)
	v_mfma_f32_32x32x16_f16 v[50:65], v[130:133], v[118:121], v[50:65]
	s_waitcnt lgkmcnt(1)
	v_mfma_f32_32x32x16_f16 v[34:49], v[134:137], v[118:121], v[34:49]
	v_mfma_f32_32x32x16_f16 v[2:17], v[114:117], v[130:133], v[2:17]
	v_mfma_f32_32x32x16_f16 v[18:33], v[114:117], v[134:137], v[18:33]
	ds_read_b128 v[130:133], v159 offset:8768
	ds_read_b128 v[134:137], v159 offset:96
	s_waitcnt vmcnt(6) lgkmcnt(2)
	v_mfma_f32_32x32x16_f16 v[50:65], v[160:163], v[110:113], v[50:65]
	s_waitcnt lgkmcnt(1)
	v_mfma_f32_32x32x16_f16 v[34:49], v[130:133], v[110:113], v[34:49]
	v_mfma_f32_32x32x16_f16 v[2:17], v[106:109], v[160:163], v[2:17]
	v_mfma_f32_32x32x16_f16 v[18:33], v[106:109], v[130:133], v[18:33]
	ds_read_b128 v[130:133], v159 offset:8800
	ds_read_b128 v[160:163], v159 offset:128
	s_waitcnt vmcnt(4) lgkmcnt(2)
	v_mfma_f32_32x32x16_f16 v[50:65], v[134:137], v[102:105], v[50:65]
	s_waitcnt lgkmcnt(1)
	v_mfma_f32_32x32x16_f16 v[34:49], v[130:133], v[102:105], v[34:49]
	v_mfma_f32_32x32x16_f16 v[2:17], v[98:101], v[134:137], v[2:17]
	v_mfma_f32_32x32x16_f16 v[18:33], v[98:101], v[130:133], v[18:33]
	ds_read_b128 v[130:133], v159 offset:8832
	ds_read_b128 v[134:137], v159 offset:160
	s_waitcnt vmcnt(3) lgkmcnt(2)
	v_mfma_f32_32x32x16_f16 v[50:65], v[160:163], v[94:97], v[50:65]
	s_waitcnt lgkmcnt(1)
	v_mfma_f32_32x32x16_f16 v[34:49], v[130:133], v[94:97], v[34:49]
	v_mfma_f32_32x32x16_f16 v[2:17], v[86:89], v[160:163], v[2:17]
	v_mfma_f32_32x32x16_f16 v[18:33], v[86:89], v[130:133], v[18:33]
	ds_read_b128 v[130:133], v159 offset:8864
	ds_read_b128 v[160:163], v159 offset:192
	s_waitcnt vmcnt(2) lgkmcnt(2)
	v_mfma_f32_32x32x16_f16 v[50:65], v[134:137], v[90:93], v[50:65]
	s_waitcnt lgkmcnt(1)
	v_mfma_f32_32x32x16_f16 v[34:49], v[130:133], v[90:93], v[34:49]
	v_mfma_f32_32x32x16_f16 v[2:17], v[78:81], v[134:137], v[2:17]
	v_mfma_f32_32x32x16_f16 v[18:33], v[78:81], v[130:133], v[18:33]
	ds_read_b128 v[130:133], v159 offset:8896
	ds_read_b128 v[164:167], v159 offset:224
	s_waitcnt vmcnt(1) lgkmcnt(2)
	v_mfma_f32_32x32x16_f16 v[50:65], v[160:163], v[82:85], v[50:65]
	s_waitcnt lgkmcnt(1)
	v_mfma_f32_32x32x16_f16 v[34:49], v[130:133], v[82:85], v[34:49]
	v_mfma_f32_32x32x16_f16 v[2:17], v[70:73], v[160:163], v[2:17]
	v_mfma_f32_32x32x16_f16 v[18:33], v[70:73], v[130:133], v[18:33]
	v_lshlrev_b32_e32 v130, 3, v138
	v_and_b32_e32 v241, 0x1f8, v130
	global_load_dwordx2 v[138:139], v241, s[0:1]
	global_load_dwordx2 v[134:135], v241, s[0:1] offset:512
	global_load_dwordx2 v[132:133], v241, s[0:1] offset:1024
	global_load_dwordx2 v[130:131], v241, s[0:1] offset:1536
	global_load_dwordx2 v[136:137], v241, s[0:1] offset:2048
	s_waitcnt vmcnt(5) lgkmcnt(0)
	v_mfma_f32_32x32x16_f16 v[50:65], v[164:167], v[74:77], v[50:65]
	v_mfma_f32_32x32x16_f16 v[2:17], v[66:69], v[164:167], v[2:17]
	s_nop 10
	v_cvt_pk_f16_f32 v57, v56, v57
	v_cvt_pk_f16_f32 v56, v54, v55
	v_cvt_pk_f16_f32 v55, v52, v53
	v_cvt_pk_f16_f32 v54, v50, v51
	v_perm_b32 v50, v240, v154, s42
	v_perm_b32 v51, v240, v154, s43
	v_perm_b32 v52, v240, v155, s42
	v_perm_b32 v53, v240, v155, s43
	v_pk_add_f16 v50, v50, s3 op_sel_hi:[1,0]
	v_pk_add_f16 v51, v51, s3 op_sel_hi:[1,0]
	v_pk_add_f16 v52, v52, s3 op_sel_hi:[1,0]
	v_pk_add_f16 v53, v53, s3 op_sel_hi:[1,0]
	v_cvt_pk_f16_f32 v65, v64, v65
	v_cvt_pk_f16_f32 v64, v62, v63
	v_cvt_pk_f16_f32 v63, v60, v61
	v_cvt_pk_f16_f32 v62, v58, v59
	v_mfma_f32_32x32x16_f16 v[2:17], v[54:57], v[50:53], v[2:17]
	v_perm_b32 v58, v240, v150, s42
	v_perm_b32 v59, v240, v150, s43
	v_perm_b32 v60, v240, v151, s42
	v_perm_b32 v61, v240, v151, s43
	v_pk_add_f16 v58, v58, s3 op_sel_hi:[1,0]
	v_pk_add_f16 v59, v59, s3 op_sel_hi:[1,0]
	v_pk_add_f16 v60, v60, s3 op_sel_hi:[1,0]
	v_pk_add_f16 v61, v61, s3 op_sel_hi:[1,0]
	s_nop 1
	v_mfma_f32_32x32x16_f16 v[2:17], v[62:65], v[58:61], v[2:17]
	ds_read_b128 v[160:163], v159 offset:8928
	v_perm_b32 v155, v240, v152, s43
	v_perm_b32 v164, v240, v153, s42
	s_waitcnt lgkmcnt(0)
	v_mfma_f32_32x32x16_f16 v[18:33], v[66:69], v[160:163], v[18:33]
	v_perm_b32 v154, v240, v152, s42
	v_perm_b32 v165, v240, v153, s43
	v_pk_add_f16 v152, v154, s3 op_sel_hi:[1,0]
	v_pk_add_f16 v153, v155, s3 op_sel_hi:[1,0]
	v_pk_add_f16 v154, v164, s3 op_sel_hi:[1,0]
	v_pk_add_f16 v155, v165, s3 op_sel_hi:[1,0]
	v_mfma_f32_32x32x16_f16 v[34:49], v[160:163], v[74:77], v[34:49]
	v_perm_b32 v151, v240, v148, s43
	v_perm_b32 v164, v240, v149, s42
	v_mfma_f32_32x32x16_f16 v[18:33], v[54:57], v[152:155], v[18:33]
	v_perm_b32 v150, v240, v148, s42
	v_perm_b32 v165, v240, v149, s43
	v_pk_add_f16 v148, v150, s3 op_sel_hi:[1,0]
	v_pk_add_f16 v149, v151, s3 op_sel_hi:[1,0]
	v_pk_add_f16 v150, v164, s3 op_sel_hi:[1,0]
	v_pk_add_f16 v151, v165, s3 op_sel_hi:[1,0]
	s_nop 2
	v_cvt_pk_f16_f32 v41, v40, v41
	v_cvt_pk_f16_f32 v40, v38, v39
	v_cvt_pk_f16_f32 v38, v34, v35
	v_cvt_pk_f16_f32 v39, v36, v37
	v_mfma_f32_32x32x16_f16 v[18:33], v[62:65], v[148:151], v[18:33]
	v_perm_b32 v34, v240, v146, s42
	v_perm_b32 v35, v240, v146, s43
	v_perm_b32 v36, v240, v147, s42
	v_perm_b32 v37, v240, v147, s43
	v_pk_add_f16 v34, v34, s3 op_sel_hi:[1,0]
	v_pk_add_f16 v35, v35, s3 op_sel_hi:[1,0]
	v_pk_add_f16 v36, v36, s3 op_sel_hi:[1,0]
	v_pk_add_f16 v37, v37, s3 op_sel_hi:[1,0]
	v_perm_b32 v146, v240, v144, s42
	v_perm_b32 v144, v240, v144, s43
	v_perm_b32 v147, v240, v145, s42
	v_perm_b32 v53, v240, v145, s43
	v_pk_add_f16 v50, v146, s3 op_sel_hi:[1,0]
	v_pk_add_f16 v51, v144, s3 op_sel_hi:[1,0]
	v_pk_add_f16 v52, v147, s3 op_sel_hi:[1,0]
	v_pk_add_f16 v53, v53, s3 op_sel_hi:[1,0]
	v_cvt_pk_f16_f32 v49, v48, v49
	v_cvt_pk_f16_f32 v48, v46, v47
	v_cvt_pk_f16_f32 v47, v44, v45
	v_mfma_f32_32x32x16_f16 v[2:17], v[38:41], v[34:37], v[2:17]
	v_cvt_pk_f16_f32 v46, v42, v43
	v_mfma_f32_32x32x16_f16 v[18:33], v[38:41], v[50:53], v[18:33]
	v_perm_b32 v34, v240, v140, s42
	v_perm_b32 v35, v240, v140, s43
	v_perm_b32 v36, v240, v141, s42
	v_perm_b32 v37, v240, v141, s43
	v_perm_b32 v42, v240, v142, s42
	v_perm_b32 v43, v240, v142, s43
	v_perm_b32 v44, v240, v143, s42
	v_perm_b32 v45, v240, v143, s43
	v_pk_add_f16 v34, v34, s3 op_sel_hi:[1,0]
	v_pk_add_f16 v35, v35, s3 op_sel_hi:[1,0]
	v_pk_add_f16 v36, v36, s3 op_sel_hi:[1,0]
	v_pk_add_f16 v37, v37, s3 op_sel_hi:[1,0]
	v_pk_add_f16 v42, v42, s3 op_sel_hi:[1,0]
	v_pk_add_f16 v43, v43, s3 op_sel_hi:[1,0]
	v_pk_add_f16 v44, v44, s3 op_sel_hi:[1,0]
	v_pk_add_f16 v45, v45, s3 op_sel_hi:[1,0]
	v_mfma_f32_32x32x16_f16 v[18:33], v[46:49], v[34:37], v[18:33]
	global_load_dwordx2 v[154:155], v241, s[0:1] offset:2560
	global_load_dwordx2 v[152:153], v241, s[0:1] offset:3072
	global_load_dwordx2 v[150:151], v241, s[0:1] offset:3584
	v_mov_b32_e32 v148, v0
	s_or_b32 s0, s10, 4
	s_ashr_i32 s1, s0, 31
	s_lshl_b64 s[0:1], s[0:1], 12
	v_mfma_f32_32x32x16_f16 v[2:17], v[46:49], v[42:45], v[2:17]
	s_nop 7
	s_nop 4
	v_cvt_pk_f16_f32 v254, v2, v3
	v_cvt_pk_f16_f32 v255, v4, v5
	ds_write_b64 v251, v[254:255] offset:0
	v_mov_b32_e32 v222, v2
	v_mov_b32_e32 v223, v3
	v_pk_mul_f32 v[194:195], v[2:3], v[2:3]
	v_mov_b32_e32 v220, v4
	v_mov_b32_e32 v221, v5
	v_pk_mul_f32 v[192:193], v[4:5], v[4:5]
	v_cvt_pk_f16_f32 v252, v6, v7
	v_cvt_pk_f16_f32 v253, v8, v9
	ds_write_b64 v251, v[252:253] offset:16
	v_mov_b32_e32 v218, v6
	v_mov_b32_e32 v219, v7
	v_pk_mul_f32 v[184:185], v[6:7], v[6:7]
	v_mov_b32_e32 v216, v8
	v_mov_b32_e32 v217, v9
	v_pk_mul_f32 v[166:167], v[8:9], v[8:9]
	v_cvt_pk_f16_f32 v254, v10, v11
	v_cvt_pk_f16_f32 v255, v12, v13
	ds_write_b64 v251, v[254:255] offset:32
	v_mov_b32_e32 v214, v10
	v_mov_b32_e32 v215, v11
	v_pk_mul_f32 v[164:165], v[10:11], v[10:11]
	v_mov_b32_e32 v204, v12
	v_mov_b32_e32 v205, v13
	v_pk_mul_f32 v[162:163], v[12:13], v[12:13]
	v_cvt_pk_f16_f32 v252, v14, v15
	v_cvt_pk_f16_f32 v253, v16, v17
	ds_write_b64 v251, v[252:253] offset:48
	v_mov_b32_e32 v202, v14
	v_mov_b32_e32 v203, v15
	v_pk_mul_f32 v[160:161], v[14:15], v[14:15]
	v_mov_b32_e32 v196, v16
	v_mov_b32_e32 v197, v17
	v_pk_mul_f32 v[156:157], v[16:17], v[16:17]
	v_cvt_pk_f16_f32 v254, v18, v19
	v_cvt_pk_f16_f32 v255, v20, v21
	ds_write_b64 v251, v[254:255] offset:4608
	v_pk_add_f32 v[222:223], v[222:223], v[18:19]
	v_pk_fma_f32 v[194:195], v[18:19], v[18:19], v[194:195]
	v_pk_add_f32 v[220:221], v[220:221], v[20:21]
	v_pk_fma_f32 v[192:193], v[20:21], v[20:21], v[192:193]
	v_cvt_pk_f16_f32 v252, v22, v23
	v_cvt_pk_f16_f32 v253, v24, v25
	ds_write_b64 v251, v[252:253] offset:4624
	v_pk_add_f32 v[218:219], v[218:219], v[22:23]
	v_pk_fma_f32 v[184:185], v[22:23], v[22:23], v[184:185]
	v_pk_add_f32 v[216:217], v[216:217], v[24:25]
	v_pk_fma_f32 v[166:167], v[24:25], v[24:25], v[166:167]
	v_cvt_pk_f16_f32 v254, v26, v27
	v_cvt_pk_f16_f32 v255, v28, v29
	ds_write_b64 v251, v[254:255] offset:4640
	v_pk_add_f32 v[214:215], v[214:215], v[26:27]
	v_pk_fma_f32 v[164:165], v[26:27], v[26:27], v[164:165]
	v_pk_add_f32 v[204:205], v[204:205], v[28:29]
	v_pk_fma_f32 v[162:163], v[28:29], v[28:29], v[162:163]
	v_cvt_pk_f16_f32 v252, v30, v31
	v_cvt_pk_f16_f32 v253, v32, v33
	ds_write_b64 v251, v[252:253] offset:4656
	v_pk_add_f32 v[202:203], v[202:203], v[30:31]
	v_pk_fma_f32 v[160:161], v[30:31], v[30:31], v[160:161]
	v_pk_add_f32 v[196:197], v[196:197], v[32:33]
	v_pk_fma_f32 v[156:157], v[32:33], v[32:33], v[156:157]
	s_nop 3
	s_nop 0
	s_waitcnt lgkmcnt(0)
	s_barrier
	s_nop 4
	ds_read_b128 v[2:5], v159 offset:34816
	ds_read_b128 v[18:21], v159 offset:43520
	ds_read_b128 v[140:143], v159 offset:34848
	ds_read_b128 v[144:147], v159 offset:43552
	s_waitcnt lgkmcnt(3)
	v_mfma_f32_32x32x16_f16 v[50:65], v[2:5], v[126:129], 0
	s_add_u32 s0, s8, s0
	s_addc_u32 s1, s9, s1
	s_waitcnt lgkmcnt(2)
	v_mfma_f32_32x32x16_f16 v[34:49], v[18:21], v[126:129], 0
	v_mfma_f32_32x32x16_f16 v[2:17], v[122:125], v[2:5], v[168:183]
	v_mfma_f32_32x32x16_f16 v[18:33], v[122:125], v[18:21], v[168:183]
	ds_read_b128 v[242:245], v159 offset:34880
	ds_read_b128 v[246:249], v159 offset:43584
	s_waitcnt lgkmcnt(3)
	v_mfma_f32_32x32x16_f16 v[50:65], v[140:143], v[118:121], v[50:65]
	s_waitcnt lgkmcnt(2)
	v_mfma_f32_32x32x16_f16 v[34:49], v[144:147], v[118:121], v[34:49]
	v_mfma_f32_32x32x16_f16 v[2:17], v[114:117], v[140:143], v[2:17]
	v_mfma_f32_32x32x16_f16 v[18:33], v[114:117], v[144:147], v[18:33]
	ds_read_b128 v[140:143], v159 offset:34912
	ds_read_b128 v[144:147], v159 offset:43616
	s_waitcnt lgkmcnt(3)
	v_mfma_f32_32x32x16_f16 v[50:65], v[242:245], v[110:113], v[50:65]
	s_waitcnt lgkmcnt(2)
	v_mfma_f32_32x32x16_f16 v[34:49], v[246:249], v[110:113], v[34:49]
	v_mfma_f32_32x32x16_f16 v[2:17], v[106:109], v[242:245], v[2:17]
	v_mfma_f32_32x32x16_f16 v[18:33], v[106:109], v[246:249], v[18:33]
	ds_read_b128 v[242:245], v159 offset:34944
	ds_read_b128 v[246:249], v159 offset:43648
	s_waitcnt lgkmcnt(3)
	v_mfma_f32_32x32x16_f16 v[50:65], v[140:143], v[102:105], v[50:65]
	s_waitcnt lgkmcnt(2)
	v_mfma_f32_32x32x16_f16 v[34:49], v[144:147], v[102:105], v[34:49]
	v_mfma_f32_32x32x16_f16 v[2:17], v[98:101], v[140:143], v[2:17]
	v_mfma_f32_32x32x16_f16 v[18:33], v[98:101], v[144:147], v[18:33]
	ds_read_b128 v[186:189], v159 offset:34976
	ds_read_b128 v[206:209], v159 offset:43680
	s_waitcnt lgkmcnt(3)
	v_mfma_f32_32x32x16_f16 v[50:65], v[242:245], v[94:97], v[50:65]
	s_waitcnt lgkmcnt(2)
	v_mfma_f32_32x32x16_f16 v[34:49], v[246:249], v[94:97], v[34:49]
	v_mfma_f32_32x32x16_f16 v[2:17], v[86:89], v[242:245], v[2:17]
	v_mfma_f32_32x32x16_f16 v[18:33], v[86:89], v[246:249], v[18:33]
	ds_read_b128 v[140:143], v159 offset:35008
	ds_read_b128 v[144:147], v159 offset:43712
	s_waitcnt lgkmcnt(3)
	v_mfma_f32_32x32x16_f16 v[50:65], v[186:189], v[90:93], v[50:65]
	s_waitcnt lgkmcnt(2)
	v_mfma_f32_32x32x16_f16 v[34:49], v[206:209], v[90:93], v[34:49]
	v_mfma_f32_32x32x16_f16 v[2:17], v[78:81], v[186:189], v[2:17]
	v_mfma_f32_32x32x16_f16 v[18:33], v[78:81], v[206:209], v[18:33]
	ds_read_b128 v[186:189], v159 offset:35040
	ds_read_b128 v[206:209], v159 offset:43744
	s_waitcnt lgkmcnt(3)
	v_mfma_f32_32x32x16_f16 v[50:65], v[140:143], v[82:85], v[50:65]
	s_waitcnt lgkmcnt(2)
	v_mfma_f32_32x32x16_f16 v[34:49], v[144:147], v[82:85], v[34:49]
	v_mfma_f32_32x32x16_f16 v[2:17], v[70:73], v[140:143], v[2:17]
	v_lshlrev_b32_e32 v140, 3, v148
	v_and_b32_e32 v199, 0x1f8, v140
	global_load_dwordx2 v[148:149], v199, s[0:1]
	global_load_dwordx2 v[142:143], v199, s[0:1] offset:1024
	global_load_dwordx2 v[140:141], v199, s[0:1] offset:1536
	v_mfma_f32_32x32x16_f16 v[18:33], v[70:73], v[144:147], v[18:33]
	global_load_dwordx2 v[144:145], v199, s[0:1] offset:512
	global_load_dwordx2 v[146:147], v199, s[0:1] offset:2048
	s_waitcnt lgkmcnt(1)
	v_mfma_f32_32x32x16_f16 v[50:65], v[186:189], v[74:77], v[50:65]
	v_mfma_f32_32x32x16_f16 v[2:17], v[66:69], v[186:189], v[2:17]
	s_nop 10
	v_cvt_pk_f16_f32 v57, v56, v57
	v_cvt_pk_f16_f32 v56, v54, v55
	v_cvt_pk_f16_f32 v54, v50, v51
	s_waitcnt vmcnt(12)
	v_cvt_pk_f16_f32 v55, v52, v53
	s_waitcnt vmcnt(8)
	v_perm_b32 v50, v240, v138, s42
	v_perm_b32 v51, v240, v138, s43
	v_perm_b32 v52, v240, v139, s42
	v_perm_b32 v53, v240, v139, s43
	v_perm_b32 v139, v240, v136, s43
	v_pk_add_f16 v50, v50, s3 op_sel_hi:[1,0]
	v_pk_add_f16 v51, v51, s3 op_sel_hi:[1,0]
	v_pk_add_f16 v52, v52, s3 op_sel_hi:[1,0]
	v_pk_add_f16 v53, v53, s3 op_sel_hi:[1,0]
	v_perm_b32 v190, v240, v137, s42
	s_waitcnt lgkmcnt(0)
	v_mfma_f32_32x32x16_f16 v[18:33], v[66:69], v[206:209], v[18:33]
	v_perm_b32 v138, v240, v136, s42
	v_perm_b32 v191, v240, v137, s43
	v_pk_add_f16 v136, v138, s3 op_sel_hi:[1,0]
	v_pk_add_f16 v137, v139, s3 op_sel_hi:[1,0]
	v_pk_add_f16 v138, v190, s3 op_sel_hi:[1,0]
	v_pk_add_f16 v139, v191, s3 op_sel_hi:[1,0]
	v_cvt_pk_f16_f32 v65, v64, v65
	v_cvt_pk_f16_f32 v64, v62, v63
	v_cvt_pk_f16_f32 v63, v60, v61
	v_cvt_pk_f16_f32 v62, v58, v59
	v_mfma_f32_32x32x16_f16 v[34:49], v[206:209], v[74:77], v[34:49]
	v_mfma_f32_32x32x16_f16 v[2:17], v[54:57], v[50:53], v[2:17]
	s_waitcnt vmcnt(7)
	v_perm_b32 v58, v240, v134, s42
	v_perm_b32 v59, v240, v134, s43
	v_perm_b32 v60, v240, v135, s42
	v_perm_b32 v61, v240, v135, s43
	v_pk_add_f16 v58, v58, s3 op_sel_hi:[1,0]
	v_pk_add_f16 v59, v59, s3 op_sel_hi:[1,0]
	v_pk_add_f16 v60, v60, s3 op_sel_hi:[1,0]
	v_pk_add_f16 v61, v61, s3 op_sel_hi:[1,0]
	v_mfma_f32_32x32x16_f16 v[18:33], v[54:57], v[136:139], v[18:33]
	v_perm_b32 v134, v240, v154, s42
	v_perm_b32 v135, v240, v154, s43
	v_perm_b32 v154, v240, v155, s42
	v_perm_b32 v155, v240, v155, s43
	v_pk_add_f16 v210, v134, s3 op_sel_hi:[1,0]
	v_pk_add_f16 v211, v135, s3 op_sel_hi:[1,0]
	v_pk_add_f16 v212, v154, s3 op_sel_hi:[1,0]
	v_pk_add_f16 v213, v155, s3 op_sel_hi:[1,0]
	v_cvt_pk_f16_f32 v41, v40, v41
	v_cvt_pk_f16_f32 v40, v38, v39
	v_cvt_pk_f16_f32 v39, v36, v37
	v_cvt_pk_f16_f32 v38, v34, v35
	v_mfma_f32_32x32x16_f16 v[2:17], v[62:65], v[58:61], v[2:17]
	v_perm_b32 v34, v240, v132, s42
	v_perm_b32 v35, v240, v132, s43
	v_perm_b32 v36, v240, v133, s42
	v_perm_b32 v37, v240, v133, s43
	v_pk_add_f16 v34, v34, s3 op_sel_hi:[1,0]
	v_pk_add_f16 v35, v35, s3 op_sel_hi:[1,0]
	v_pk_add_f16 v36, v36, s3 op_sel_hi:[1,0]
	v_pk_add_f16 v37, v37, s3 op_sel_hi:[1,0]
	s_waitcnt vmcnt(6)
	v_mfma_f32_32x32x16_f16 v[18:33], v[62:65], v[210:213], v[18:33]
	v_perm_b32 v132, v240, v152, s42
	v_perm_b32 v133, v240, v152, s43
	v_perm_b32 v134, v240, v153, s42
	v_perm_b32 v53, v240, v153, s43
	v_pk_add_f16 v50, v132, s3 op_sel_hi:[1,0]
	v_pk_add_f16 v51, v133, s3 op_sel_hi:[1,0]
	v_pk_add_f16 v52, v134, s3 op_sel_hi:[1,0]
	v_pk_add_f16 v53, v53, s3 op_sel_hi:[1,0]
	v_cvt_pk_f16_f32 v49, v48, v49
	v_cvt_pk_f16_f32 v48, v46, v47
	v_cvt_pk_f16_f32 v47, v44, v45
	v_cvt_pk_f16_f32 v46, v42, v43
	v_mfma_f32_32x32x16_f16 v[2:17], v[38:41], v[34:37], v[2:17]
	v_perm_b32 v42, v240, v130, s42
	v_perm_b32 v43, v240, v130, s43
	v_perm_b32 v44, v240, v131, s42
	v_perm_b32 v45, v240, v131, s43
	v_pk_add_f16 v42, v42, s3 op_sel_hi:[1,0]
	v_pk_add_f16 v43, v43, s3 op_sel_hi:[1,0]
	v_pk_add_f16 v44, v44, s3 op_sel_hi:[1,0]
	v_pk_add_f16 v45, v45, s3 op_sel_hi:[1,0]
	s_waitcnt vmcnt(5)
	v_mfma_f32_32x32x16_f16 v[18:33], v[38:41], v[50:53], v[18:33]
	v_perm_b32 v34, v240, v150, s42
	v_perm_b32 v35, v240, v150, s43
	v_perm_b32 v36, v240, v151, s42
	v_perm_b32 v37, v240, v151, s43
	v_pk_add_f16 v34, v34, s3 op_sel_hi:[1,0]
	v_pk_add_f16 v35, v35, s3 op_sel_hi:[1,0]
	v_pk_add_f16 v36, v36, s3 op_sel_hi:[1,0]
	v_pk_add_f16 v37, v37, s3 op_sel_hi:[1,0]
	v_mfma_f32_32x32x16_f16 v[2:17], v[46:49], v[42:45], v[2:17]
	global_load_dwordx2 v[154:155], v199, s[0:1] offset:2560
	global_load_dwordx2 v[152:153], v199, s[0:1] offset:3072
	global_load_dwordx2 v[150:151], v199, s[0:1] offset:3584
	s_or_b32 s0, s10, 6
	s_ashr_i32 s1, s0, 31
	s_lshl_b64 s[0:1], s[0:1], 12
	s_add_u32 s0, s8, s0
	v_mfma_f32_32x32x16_f16 v[18:33], v[46:49], v[34:37], v[18:33]
	s_nop 7
	s_nop 4
	v_cvt_pk_f16_f32 v254, v2, v3
	v_cvt_pk_f16_f32 v255, v4, v5
	ds_write_b64 v251, v[254:255] offset:18432
	v_pk_add_f32 v[222:223], v[222:223], v[2:3]
	v_pk_fma_f32 v[194:195], v[2:3], v[2:3], v[194:195]
	v_pk_add_f32 v[220:221], v[220:221], v[4:5]
	v_pk_fma_f32 v[192:193], v[4:5], v[4:5], v[192:193]
	v_cvt_pk_f16_f32 v252, v6, v7
	v_cvt_pk_f16_f32 v253, v8, v9
	ds_write_b64 v251, v[252:253] offset:18448
	v_pk_add_f32 v[218:219], v[218:219], v[6:7]
	v_pk_fma_f32 v[184:185], v[6:7], v[6:7], v[184:185]
	v_pk_add_f32 v[216:217], v[216:217], v[8:9]
	v_pk_fma_f32 v[166:167], v[8:9], v[8:9], v[166:167]
	v_cvt_pk_f16_f32 v254, v10, v11
	v_cvt_pk_f16_f32 v255, v12, v13
	ds_write_b64 v251, v[254:255] offset:18464
	v_pk_add_f32 v[214:215], v[214:215], v[10:11]
	v_pk_fma_f32 v[164:165], v[10:11], v[10:11], v[164:165]
	v_pk_add_f32 v[204:205], v[204:205], v[12:13]
	v_pk_fma_f32 v[162:163], v[12:13], v[12:13], v[162:163]
	v_cvt_pk_f16_f32 v252, v14, v15
	v_cvt_pk_f16_f32 v253, v16, v17
	ds_write_b64 v251, v[252:253] offset:18480
	v_pk_add_f32 v[202:203], v[202:203], v[14:15]
	v_pk_fma_f32 v[160:161], v[14:15], v[14:15], v[160:161]
	v_pk_add_f32 v[196:197], v[196:197], v[16:17]
	v_pk_fma_f32 v[156:157], v[16:17], v[16:17], v[156:157]
	v_cvt_pk_f16_f32 v254, v18, v19
	v_cvt_pk_f16_f32 v255, v20, v21
	ds_write_b64 v251, v[254:255] offset:23040
	v_pk_add_f32 v[222:223], v[222:223], v[18:19]
	v_pk_fma_f32 v[194:195], v[18:19], v[18:19], v[194:195]
	v_pk_add_f32 v[220:221], v[220:221], v[20:21]
	v_pk_fma_f32 v[192:193], v[20:21], v[20:21], v[192:193]
	v_cvt_pk_f16_f32 v252, v22, v23
	v_cvt_pk_f16_f32 v253, v24, v25
	ds_write_b64 v251, v[252:253] offset:23056
	v_pk_add_f32 v[218:219], v[218:219], v[22:23]
	v_pk_fma_f32 v[184:185], v[22:23], v[22:23], v[184:185]
	v_pk_add_f32 v[216:217], v[216:217], v[24:25]
	v_pk_fma_f32 v[166:167], v[24:25], v[24:25], v[166:167]
	v_cvt_pk_f16_f32 v254, v26, v27
	v_cvt_pk_f16_f32 v255, v28, v29
	ds_write_b64 v251, v[254:255] offset:23072
	v_pk_add_f32 v[214:215], v[214:215], v[26:27]
	v_pk_fma_f32 v[164:165], v[26:27], v[26:27], v[164:165]
	v_pk_add_f32 v[204:205], v[204:205], v[28:29]
	v_pk_fma_f32 v[162:163], v[28:29], v[28:29], v[162:163]
	v_cvt_pk_f16_f32 v252, v30, v31
	v_cvt_pk_f16_f32 v253, v32, v33
	ds_write_b64 v251, v[252:253] offset:23088
	v_pk_add_f32 v[202:203], v[202:203], v[30:31]
	v_pk_fma_f32 v[160:161], v[30:31], v[30:31], v[160:161]
	v_pk_add_f32 v[196:197], v[196:197], v[32:33]
	v_pk_fma_f32 v[156:157], v[32:33], v[32:33], v[156:157]
	s_nop 3
	s_nop 0
	s_nop 0
	s_waitcnt lgkmcnt(0)
	s_barrier
	ds_read_b128 v[2:5], v159
	s_nop 2
	ds_read_b128 v[18:21], v159 offset:8704
	s_waitcnt lgkmcnt(1)
	v_mfma_f32_32x32x16_f16 v[50:65], v[2:5], v[126:129], 0
	v_lshlrev_b32_e32 v0, 3, v0
	s_addc_u32 s1, s9, s1
	v_and_b32_e32 v0, 0x1f8, v0
	global_load_dwordx2 v[138:139], v0, s[0:1]
	s_waitcnt lgkmcnt(0)
	v_mfma_f32_32x32x16_f16 v[34:49], v[18:21], v[126:129], 0
	v_mfma_f32_32x32x16_f16 v[2:17], v[122:125], v[2:5], v[168:183]
	v_mfma_f32_32x32x16_f16 v[18:33], v[122:125], v[18:21], v[168:183]
	ds_read_b128 v[130:133], v159 offset:32
	ds_read_b128 v[134:137], v159 offset:8736
	s_waitcnt lgkmcnt(1)
	v_mfma_f32_32x32x16_f16 v[50:65], v[130:133], v[118:121], v[50:65]
	s_waitcnt lgkmcnt(0)
	v_mfma_f32_32x32x16_f16 v[34:49], v[134:137], v[118:121], v[34:49]
	v_mfma_f32_32x32x16_f16 v[2:17], v[114:117], v[130:133], v[2:17]
	v_mfma_f32_32x32x16_f16 v[18:33], v[114:117], v[134:137], v[18:33]
	ds_read_b128 v[224:227], v159 offset:64
	ds_read_b128 v[228:231], v159 offset:8768
	ds_read_b128 v[130:133], v159 offset:96
	ds_read_b128 v[134:137], v159 offset:8800
	s_waitcnt lgkmcnt(3)
	v_mfma_f32_32x32x16_f16 v[50:65], v[224:227], v[110:113], v[50:65]
	s_waitcnt lgkmcnt(2)
	v_mfma_f32_32x32x16_f16 v[34:49], v[228:231], v[110:113], v[34:49]
	v_mfma_f32_32x32x16_f16 v[2:17], v[106:109], v[224:227], v[2:17]
	v_mfma_f32_32x32x16_f16 v[18:33], v[106:109], v[228:231], v[18:33]
	ds_read_b128 v[224:227], v159 offset:128
	ds_read_b128 v[228:231], v159 offset:8832
	s_waitcnt lgkmcnt(3)
	v_mfma_f32_32x32x16_f16 v[50:65], v[130:133], v[102:105], v[50:65]
	s_waitcnt lgkmcnt(2)
	v_mfma_f32_32x32x16_f16 v[34:49], v[134:137], v[102:105], v[34:49]
	v_mfma_f32_32x32x16_f16 v[2:17], v[98:101], v[130:133], v[2:17]
	v_mfma_f32_32x32x16_f16 v[18:33], v[98:101], v[134:137], v[18:33]
	ds_read_b128 v[130:133], v159 offset:160
	ds_read_b128 v[134:137], v159 offset:8864
	s_waitcnt lgkmcnt(3)
	v_mfma_f32_32x32x16_f16 v[50:65], v[224:227], v[94:97], v[50:65]
	s_waitcnt lgkmcnt(2)
	v_mfma_f32_32x32x16_f16 v[34:49], v[228:231], v[94:97], v[34:49]
	v_mfma_f32_32x32x16_f16 v[2:17], v[86:89], v[224:227], v[2:17]
	v_mfma_f32_32x32x16_f16 v[18:33], v[86:89], v[228:231], v[18:33]
	ds_read_b128 v[224:227], v159 offset:192
	ds_read_b128 v[228:231], v159 offset:8896
	s_waitcnt lgkmcnt(3)
	v_mfma_f32_32x32x16_f16 v[50:65], v[130:133], v[90:93], v[50:65]
	s_waitcnt lgkmcnt(2)
	v_mfma_f32_32x32x16_f16 v[34:49], v[134:137], v[90:93], v[34:49]
	v_mfma_f32_32x32x16_f16 v[2:17], v[78:81], v[130:133], v[2:17]
	v_mfma_f32_32x32x16_f16 v[18:33], v[78:81], v[134:137], v[18:33]
	ds_read_b128 v[232:235], v159 offset:224
	ds_read_b128 v[236:239], v159 offset:8928
	s_waitcnt lgkmcnt(3)
	v_mfma_f32_32x32x16_f16 v[50:65], v[224:227], v[82:85], v[50:65]
	global_load_dwordx2 v[134:135], v0, s[0:1] offset:512
	global_load_dwordx2 v[132:133], v0, s[0:1] offset:1024
	global_load_dwordx2 v[130:131], v0, s[0:1] offset:1536
	s_waitcnt lgkmcnt(2)
	v_mfma_f32_32x32x16_f16 v[34:49], v[228:231], v[82:85], v[34:49]
	global_load_dwordx2 v[136:137], v0, s[0:1] offset:2048
	v_mfma_f32_32x32x16_f16 v[2:17], v[70:73], v[224:227], v[2:17]
	v_mfma_f32_32x32x16_f16 v[18:33], v[70:73], v[228:231], v[18:33]
	s_waitcnt lgkmcnt(1)
	v_mfma_f32_32x32x16_f16 v[50:65], v[232:235], v[74:77], v[50:65]
	v_mfma_f32_32x32x16_f16 v[2:17], v[66:69], v[232:235], v[2:17]
	s_nop 10
	v_cvt_pk_f16_f32 v57, v56, v57
	v_cvt_pk_f16_f32 v56, v54, v55
	v_cvt_pk_f16_f32 v54, v50, v51
	s_waitcnt vmcnt(12)
	v_lshlrev_b32_e32 v50, 8, v148
	v_cvt_pk_f16_f32 v55, v52, v53
	v_perm_b32 v50, v50, v148, s2
	v_lshrrev_b32_e32 v51, 16, v148
	v_lshrrev_b32_e32 v52, 8, v148
	v_lshrrev_b32_e32 v53, 16, v149
	v_lshrrev_b32_e32 v148, 8, v149
	v_perm_b32 v51, v52, v51, s2
	v_lshlrev_b32_e32 v52, 8, v149
	v_perm_b32 v53, v148, v53, s2
	s_waitcnt vmcnt(8)
	v_perm_b32 v52, v52, v149, s2
	v_perm_b32 v149, v240, v146, s43
	v_perm_b32 v198, v240, v147, s42
	s_waitcnt lgkmcnt(0)
	v_mfma_f32_32x32x16_f16 v[18:33], v[66:69], v[236:239], v[18:33]
	v_or_b32_e32 v50, 0x64006400, v50
	v_or_b32_e32 v51, 0x64006400, v51
	v_or_b32_e32 v52, 0x64006400, v52
	v_or_b32_e32 v53, 0x64006400, v53
	v_pk_add_f16 v50, v50, s3 op_sel_hi:[1,0]
	v_pk_add_f16 v51, v51, s3 op_sel_hi:[1,0]
	v_pk_add_f16 v52, v52, s3 op_sel_hi:[1,0]
	v_pk_add_f16 v53, v53, s3 op_sel_hi:[1,0]
	v_perm_b32 v148, v240, v146, s42
	v_perm_b32 v200, v240, v147, s43
	v_pk_add_f16 v146, v148, s3 op_sel_hi:[1,0]
	v_pk_add_f16 v147, v149, s3 op_sel_hi:[1,0]
	v_pk_add_f16 v148, v198, s3 op_sel_hi:[1,0]
	v_pk_add_f16 v149, v200, s3 op_sel_hi:[1,0]
	v_cvt_pk_f16_f32 v65, v64, v65
	v_cvt_pk_f16_f32 v64, v62, v63
	v_cvt_pk_f16_f32 v62, v58, v59
	v_cvt_pk_f16_f32 v63, v60, v61
	s_waitcnt vmcnt(7)
	v_mfma_f32_32x32x16_f16 v[34:49], v[236:239], v[74:77], v[34:49]
	v_mfma_f32_32x32x16_f16 v[2:17], v[54:57], v[50:53], v[2:17]
	v_perm_b32 v58, v240, v144, s42
	v_perm_b32 v59, v240, v144, s43
	v_perm_b32 v60, v240, v145, s42
	v_perm_b32 v61, v240, v145, s43
	v_mfma_f32_32x32x16_f16 v[18:33], v[54:57], v[146:149], v[18:33]
	v_pk_add_f16 v58, v58, s3 op_sel_hi:[1,0]
	v_pk_add_f16 v59, v59, s3 op_sel_hi:[1,0]
	v_pk_add_f16 v60, v60, s3 op_sel_hi:[1,0]
	v_pk_add_f16 v61, v61, s3 op_sel_hi:[1,0]
	v_perm_b32 v144, v240, v154, s42
	v_perm_b32 v145, v240, v154, s43
	v_perm_b32 v154, v240, v155, s42
	v_perm_b32 v155, v240, v155, s43
	v_pk_add_f16 v224, v144, s3 op_sel_hi:[1,0]
	v_pk_add_f16 v225, v145, s3 op_sel_hi:[1,0]
	v_pk_add_f16 v226, v154, s3 op_sel_hi:[1,0]
	v_pk_add_f16 v227, v155, s3 op_sel_hi:[1,0]
	v_cvt_pk_f16_f32 v41, v40, v41
	v_cvt_pk_f16_f32 v40, v38, v39
	v_cvt_pk_f16_f32 v39, v36, v37
	v_cvt_pk_f16_f32 v38, v34, v35
	s_waitcnt vmcnt(6)
	v_mfma_f32_32x32x16_f16 v[2:17], v[62:65], v[58:61], v[2:17]
	v_perm_b32 v34, v240, v142, s42
	v_perm_b32 v35, v240, v142, s43
	v_mfma_f32_32x32x16_f16 v[18:33], v[62:65], v[224:227], v[18:33]
	v_perm_b32 v36, v240, v143, s42
	v_perm_b32 v37, v240, v143, s43
	v_pk_add_f16 v34, v34, s3 op_sel_hi:[1,0]
	v_pk_add_f16 v35, v35, s3 op_sel_hi:[1,0]
	v_pk_add_f16 v36, v36, s3 op_sel_hi:[1,0]
	v_pk_add_f16 v37, v37, s3 op_sel_hi:[1,0]
	v_perm_b32 v142, v240, v152, s42
	v_perm_b32 v143, v240, v152, s43
	v_perm_b32 v144, v240, v153, s42
	v_perm_b32 v53, v240, v153, s43
	v_pk_add_f16 v50, v142, s3 op_sel_hi:[1,0]
	v_pk_add_f16 v51, v143, s3 op_sel_hi:[1,0]
	v_pk_add_f16 v52, v144, s3 op_sel_hi:[1,0]
	v_pk_add_f16 v53, v53, s3 op_sel_hi:[1,0]
	v_cvt_pk_f16_f32 v49, v48, v49
	v_cvt_pk_f16_f32 v48, v46, v47
	v_cvt_pk_f16_f32 v47, v44, v45
	v_cvt_pk_f16_f32 v46, v42, v43
	v_mfma_f32_32x32x16_f16 v[2:17], v[38:41], v[34:37], v[2:17]
	s_waitcnt vmcnt(5)
	v_mfma_f32_32x32x16_f16 v[18:33], v[38:41], v[50:53], v[18:33]
	v_perm_b32 v42, v240, v140, s42
	v_perm_b32 v43, v240, v140, s43
	v_perm_b32 v44, v240, v141, s42
	v_perm_b32 v45, v240, v141, s43
	v_perm_b32 v34, v240, v150, s42
	v_perm_b32 v35, v240, v150, s43
	v_perm_b32 v36, v240, v151, s42
	v_perm_b32 v37, v240, v151, s43
	v_pk_add_f16 v42, v42, s3 op_sel_hi:[1,0]
	v_pk_add_f16 v43, v43, s3 op_sel_hi:[1,0]
	v_pk_add_f16 v44, v44, s3 op_sel_hi:[1,0]
	v_pk_add_f16 v45, v45, s3 op_sel_hi:[1,0]
	v_pk_add_f16 v34, v34, s3 op_sel_hi:[1,0]
	v_pk_add_f16 v35, v35, s3 op_sel_hi:[1,0]
	v_pk_add_f16 v36, v36, s3 op_sel_hi:[1,0]
	v_pk_add_f16 v37, v37, s3 op_sel_hi:[1,0]
	v_mfma_f32_32x32x16_f16 v[2:17], v[46:49], v[42:45], v[2:17]
	global_load_dwordx2 v[142:143], v0, s[0:1] offset:2560
	global_load_dwordx2 v[140:141], v0, s[0:1] offset:3072
	global_load_dwordx2 v[64:65], v0, s[0:1] offset:3584
	v_mfma_f32_32x32x16_f16 v[18:33], v[46:49], v[34:37], v[18:33]
	s_nop 7
	s_nop 4
	v_cvt_pk_f16_f32 v254, v2, v3
	v_cvt_pk_f16_f32 v255, v4, v5
	ds_write_b64 v251, v[254:255] offset:0
	v_pk_add_f32 v[222:223], v[222:223], v[2:3]
	v_pk_fma_f32 v[194:195], v[2:3], v[2:3], v[194:195]
	v_pk_add_f32 v[220:221], v[220:221], v[4:5]
	v_pk_fma_f32 v[192:193], v[4:5], v[4:5], v[192:193]
	v_cvt_pk_f16_f32 v252, v6, v7
	v_cvt_pk_f16_f32 v253, v8, v9
	ds_write_b64 v251, v[252:253] offset:16
	v_pk_add_f32 v[218:219], v[218:219], v[6:7]
	v_pk_fma_f32 v[184:185], v[6:7], v[6:7], v[184:185]
	v_pk_add_f32 v[216:217], v[216:217], v[8:9]
	v_pk_fma_f32 v[166:167], v[8:9], v[8:9], v[166:167]
	v_cvt_pk_f16_f32 v254, v10, v11
	v_cvt_pk_f16_f32 v255, v12, v13
	ds_write_b64 v251, v[254:255] offset:32
	v_pk_add_f32 v[214:215], v[214:215], v[10:11]
	v_pk_fma_f32 v[164:165], v[10:11], v[10:11], v[164:165]
	v_pk_add_f32 v[204:205], v[204:205], v[12:13]
	v_pk_fma_f32 v[162:163], v[12:13], v[12:13], v[162:163]
	v_cvt_pk_f16_f32 v252, v14, v15
	v_cvt_pk_f16_f32 v253, v16, v17
	ds_write_b64 v251, v[252:253] offset:48
	v_pk_add_f32 v[202:203], v[202:203], v[14:15]
	v_pk_fma_f32 v[160:161], v[14:15], v[14:15], v[160:161]
	v_pk_add_f32 v[196:197], v[196:197], v[16:17]
	v_pk_fma_f32 v[156:157], v[16:17], v[16:17], v[156:157]
	v_cvt_pk_f16_f32 v254, v18, v19
	v_cvt_pk_f16_f32 v255, v20, v21
	ds_write_b64 v251, v[254:255] offset:4608
	v_pk_add_f32 v[222:223], v[222:223], v[18:19]
	v_pk_fma_f32 v[194:195], v[18:19], v[18:19], v[194:195]
	v_pk_add_f32 v[220:221], v[220:221], v[20:21]
	v_pk_fma_f32 v[192:193], v[20:21], v[20:21], v[192:193]
	v_cvt_pk_f16_f32 v252, v22, v23
	v_cvt_pk_f16_f32 v253, v24, v25
	ds_write_b64 v251, v[252:253] offset:4624
	v_pk_add_f32 v[218:219], v[218:219], v[22:23]
	v_pk_fma_f32 v[184:185], v[22:23], v[22:23], v[184:185]
	v_pk_add_f32 v[216:217], v[216:217], v[24:25]
	v_pk_fma_f32 v[166:167], v[24:25], v[24:25], v[166:167]
	v_cvt_pk_f16_f32 v254, v26, v27
	v_cvt_pk_f16_f32 v255, v28, v29
	ds_write_b64 v251, v[254:255] offset:4640
	v_pk_add_f32 v[214:215], v[214:215], v[26:27]
	v_pk_fma_f32 v[164:165], v[26:27], v[26:27], v[164:165]
	v_pk_add_f32 v[204:205], v[204:205], v[28:29]
	v_pk_fma_f32 v[162:163], v[28:29], v[28:29], v[162:163]
	v_cvt_pk_f16_f32 v252, v30, v31
	v_cvt_pk_f16_f32 v253, v32, v33
	ds_write_b64 v251, v[252:253] offset:4656
	v_pk_add_f32 v[202:203], v[202:203], v[30:31]
	v_pk_fma_f32 v[160:161], v[30:31], v[30:31], v[160:161]
	v_pk_add_f32 v[196:197], v[196:197], v[32:33]
	v_pk_fma_f32 v[156:157], v[32:33], v[32:33], v[156:157]
	s_nop 7
	s_waitcnt lgkmcnt(0)
	s_barrier
	s_nop 1
	ds_read_b128 v[16:19], v159 offset:43520
	s_waitcnt lgkmcnt(0)
	v_mfma_f32_32x32x16_f16 v[32:47], v[16:19], v[126:129], 0
	ds_read_b128 v[2:5], v159 offset:34816
	s_waitcnt lgkmcnt(0)
	v_mfma_f32_32x32x16_f16 v[48:63], v[2:5], v[126:129], 0
	ds_read_b128 v[126:129], v159 offset:34848
	s_waitcnt lgkmcnt(0)
	v_mfma_f32_32x32x16_f16 v[48:63], v[126:129], v[118:121], v[48:63]
	v_mfma_f32_32x32x16_f16 v[0:15], v[122:125], v[2:5], v[168:183]
	v_mfma_f32_32x32x16_f16 v[0:15], v[114:117], v[126:129], v[0:15]
	v_mfma_f32_32x32x16_f16 v[16:31], v[122:125], v[16:19], v[168:183]
	ds_read_b128 v[122:125], v159 offset:43552
	s_waitcnt lgkmcnt(0)
	v_mfma_f32_32x32x16_f16 v[32:47], v[122:125], v[118:121], v[32:47]
	v_mfma_f32_32x32x16_f16 v[16:31], v[114:117], v[122:125], v[16:31]
	ds_read_b128 v[118:121], v159 offset:34880
	ds_read_b128 v[114:117], v159 offset:43584
	s_waitcnt lgkmcnt(1)
	v_mfma_f32_32x32x16_f16 v[48:63], v[118:121], v[110:113], v[48:63]
	s_waitcnt lgkmcnt(0)
	v_mfma_f32_32x32x16_f16 v[32:47], v[114:117], v[110:113], v[32:47]
	v_mfma_f32_32x32x16_f16 v[0:15], v[106:109], v[118:121], v[0:15]
	ds_read_b128 v[110:113], v159 offset:34912
	v_mfma_f32_32x32x16_f16 v[16:31], v[106:109], v[114:117], v[16:31]
	ds_read_b128 v[106:109], v159 offset:43616
	s_waitcnt lgkmcnt(1)
	v_mfma_f32_32x32x16_f16 v[48:63], v[110:113], v[102:105], v[48:63]
	s_waitcnt lgkmcnt(0)
	v_mfma_f32_32x32x16_f16 v[32:47], v[106:109], v[102:105], v[32:47]
	v_mfma_f32_32x32x16_f16 v[0:15], v[98:101], v[110:113], v[0:15]
	ds_read_b128 v[102:105], v159 offset:34944
	v_mfma_f32_32x32x16_f16 v[16:31], v[98:101], v[106:109], v[16:31]
	ds_read_b128 v[98:101], v159 offset:43648
	s_waitcnt lgkmcnt(1)
	v_mfma_f32_32x32x16_f16 v[48:63], v[102:105], v[94:97], v[48:63]
	s_waitcnt lgkmcnt(0)
	v_mfma_f32_32x32x16_f16 v[32:47], v[98:101], v[94:97], v[32:47]
	v_mfma_f32_32x32x16_f16 v[0:15], v[86:89], v[102:105], v[0:15]
	ds_read_b128 v[94:97], v159 offset:34976
	v_mfma_f32_32x32x16_f16 v[16:31], v[86:89], v[98:101], v[16:31]
	ds_read_b128 v[86:89], v159 offset:43680
	s_waitcnt lgkmcnt(1)
	v_mfma_f32_32x32x16_f16 v[48:63], v[94:97], v[90:93], v[48:63]
	s_waitcnt lgkmcnt(0)
	v_mfma_f32_32x32x16_f16 v[32:47], v[86:89], v[90:93], v[32:47]
	v_mfma_f32_32x32x16_f16 v[0:15], v[78:81], v[94:97], v[0:15]
	ds_read_b128 v[90:93], v159 offset:35008
	v_mfma_f32_32x32x16_f16 v[16:31], v[78:81], v[86:89], v[16:31]
	ds_read_b128 v[78:81], v159 offset:43712
	s_waitcnt lgkmcnt(1)
	v_mfma_f32_32x32x16_f16 v[48:63], v[90:93], v[82:85], v[48:63]
	s_waitcnt lgkmcnt(0)
	v_mfma_f32_32x32x16_f16 v[32:47], v[78:81], v[82:85], v[32:47]
	v_mfma_f32_32x32x16_f16 v[0:15], v[70:73], v[90:93], v[0:15]
	ds_read_b128 v[82:85], v159 offset:35040
	v_mfma_f32_32x32x16_f16 v[16:31], v[70:73], v[78:81], v[16:31]
	ds_read_b128 v[70:73], v159 offset:43744
	s_waitcnt lgkmcnt(1)
	v_mfma_f32_32x32x16_f16 v[48:63], v[82:85], v[74:77], v[48:63]
	v_mfma_f32_32x32x16_f16 v[0:15], v[66:69], v[82:85], v[0:15]
	s_nop 3
	s_nop 6
	v_cvt_pk_f16_f32 v55, v54, v55
	v_cvt_pk_f16_f32 v54, v52, v53
	v_cvt_pk_f16_f32 v53, v50, v51
	v_cvt_pk_f16_f32 v52, v48, v49
	s_waitcnt vmcnt(3)
	s_waitcnt lgkmcnt(0)
	v_mfma_f32_32x32x16_f16 v[16:31], v[66:69], v[70:73], v[16:31]
	v_lshrrev_b32_e32 v69, 16, v139
	v_mfma_f32_32x32x16_f16 v[32:47], v[70:73], v[74:77], v[32:47]
	v_lshrrev_b32_e32 v70, 8, v139
	v_perm_b32 v69, v70, v69, s2
	v_perm_b32 v66, v240, v138, s42
	v_perm_b32 v67, v240, v138, s43
	v_perm_b32 v68, v240, v139, s42
	v_or_b32_e32 v69, 0x64006400, v69
	v_pk_add_f16 v66, v66, s3 op_sel_hi:[1,0]
	v_pk_add_f16 v67, v67, s3 op_sel_hi:[1,0]
	v_pk_add_f16 v68, v68, s3 op_sel_hi:[1,0]
	v_pk_add_f16 v69, v69, s3 op_sel_hi:[1,0]
	s_nop 1
	v_mfma_f32_32x32x16_f16 v[0:15], v[52:55], v[66:69], v[0:15]
	v_perm_b32 v48, v240, v136, s42
	v_perm_b32 v49, v240, v136, s43
	v_perm_b32 v50, v240, v137, s42
	v_perm_b32 v51, v240, v137, s43
	v_pk_add_f16 v48, v48, s3 op_sel_hi:[1,0]
	v_pk_add_f16 v49, v49, s3 op_sel_hi:[1,0]
	v_pk_add_f16 v50, v50, s3 op_sel_hi:[1,0]
	v_pk_add_f16 v51, v51, s3 op_sel_hi:[1,0]
	v_cvt_pk_f16_f32 v39, v38, v39
	v_cvt_pk_f16_f32 v38, v36, v37
	v_mfma_f32_32x32x16_f16 v[16:31], v[52:55], v[48:51], v[16:31]
	v_perm_b32 v48, v240, v134, s42
	v_perm_b32 v49, v240, v134, s43
	v_perm_b32 v50, v240, v135, s42
	v_perm_b32 v51, v240, v135, s43
	v_pk_add_f16 v48, v48, s3 op_sel_hi:[1,0]
	v_pk_add_f16 v49, v49, s3 op_sel_hi:[1,0]
	v_pk_add_f16 v50, v50, s3 op_sel_hi:[1,0]
	v_pk_add_f16 v51, v51, s3 op_sel_hi:[1,0]
	v_cvt_pk_f16_f32 v55, v62, v63
	v_cvt_pk_f16_f32 v54, v60, v61
	v_cvt_pk_f16_f32 v53, v58, v59
	v_cvt_pk_f16_f32 v52, v56, v57
	s_waitcnt vmcnt(2)
	v_cvt_pk_f16_f32 v37, v34, v35
	v_mfma_f32_32x32x16_f16 v[0:15], v[52:55], v[48:51], v[0:15]
	v_perm_b32 v48, v240, v142, s42
	v_perm_b32 v49, v240, v142, s43
	v_perm_b32 v50, v240, v143, s42
	v_perm_b32 v51, v240, v143, s43
	v_pk_add_f16 v48, v48, s3 op_sel_hi:[1,0]
	v_pk_add_f16 v49, v49, s3 op_sel_hi:[1,0]
	v_pk_add_f16 v50, v50, s3 op_sel_hi:[1,0]
	v_pk_add_f16 v51, v51, s3 op_sel_hi:[1,0]
	v_cvt_pk_f16_f32 v36, v32, v33
	s_waitcnt vmcnt(1)
	v_mfma_f32_32x32x16_f16 v[16:31], v[52:55], v[48:51], v[16:31]
	v_lshrrev_b32_e32 v51, 16, v133
	v_lshrrev_b32_e32 v52, 8, v133
	v_perm_b32 v51, v52, v51, s2
	v_perm_b32 v48, v240, v132, s42
	v_perm_b32 v49, v240, v132, s43
	v_perm_b32 v50, v240, v133, s42
	v_or_b32_e32 v51, 0x64006400, v51
	v_pk_add_f16 v48, v48, s3 op_sel_hi:[1,0]
	v_pk_add_f16 v49, v49, s3 op_sel_hi:[1,0]
	v_pk_add_f16 v50, v50, s3 op_sel_hi:[1,0]
	v_pk_add_f16 v51, v51, s3 op_sel_hi:[1,0]
	s_nop 1
	v_mfma_f32_32x32x16_f16 v[0:15], v[36:39], v[48:51], v[0:15]
	v_perm_b32 v32, v240, v140, s42
	v_perm_b32 v33, v240, v140, s43
	v_perm_b32 v34, v240, v141, s42
	v_perm_b32 v35, v240, v141, s43
	v_pk_add_f16 v32, v32, s3 op_sel_hi:[1,0]
	v_pk_add_f16 v33, v33, s3 op_sel_hi:[1,0]
	v_pk_add_f16 v34, v34, s3 op_sel_hi:[1,0]
	v_pk_add_f16 v35, v35, s3 op_sel_hi:[1,0]
	s_nop 1
	v_mfma_f32_32x32x16_f16 v[16:31], v[36:39], v[32:35], v[16:31]
	v_perm_b32 v32, v240, v130, s42
	v_perm_b32 v33, v240, v130, s43
	v_perm_b32 v34, v240, v131, s42
	v_perm_b32 v35, v240, v131, s43
	v_pk_add_f16 v32, v32, s3 op_sel_hi:[1,0]
	v_pk_add_f16 v33, v33, s3 op_sel_hi:[1,0]
	v_pk_add_f16 v34, v34, s3 op_sel_hi:[1,0]
	v_pk_add_f16 v35, v35, s3 op_sel_hi:[1,0]
	v_cvt_pk_f16_f32 v39, v46, v47
	v_cvt_pk_f16_f32 v38, v44, v45
	v_cvt_pk_f16_f32 v37, v42, v43
	v_cvt_pk_f16_f32 v36, v40, v41
	s_waitcnt vmcnt(0)
	s_nop 0
	v_mfma_f32_32x32x16_f16 v[0:15], v[36:39], v[32:35], v[0:15]
	v_perm_b32 v32, v240, v64, s42
	v_perm_b32 v33, v240, v64, s43
	v_perm_b32 v34, v240, v65, s42
	v_perm_b32 v35, v240, v65, s43
	v_pk_add_f16 v32, v32, s3 op_sel_hi:[1,0]
	v_pk_add_f16 v33, v33, s3 op_sel_hi:[1,0]
	v_pk_add_f16 v34, v34, s3 op_sel_hi:[1,0]
	v_pk_add_f16 v35, v35, s3 op_sel_hi:[1,0]
	s_nop 3
	v_mfma_f32_32x32x16_f16 v[16:31], v[36:39], v[32:35], v[16:31]
	s_nop 7
	s_nop 4
	v_cvt_pk_f16_f32 v254, v0, v1
	v_cvt_pk_f16_f32 v255, v2, v3
	ds_write_b64 v251, v[254:255] offset:18432
	v_pk_add_f32 v[222:223], v[222:223], v[0:1]
	v_pk_fma_f32 v[194:195], v[0:1], v[0:1], v[194:195]
	v_pk_add_f32 v[220:221], v[220:221], v[2:3]
	v_pk_fma_f32 v[192:193], v[2:3], v[2:3], v[192:193]
	v_cvt_pk_f16_f32 v252, v4, v5
	v_cvt_pk_f16_f32 v253, v6, v7
	ds_write_b64 v251, v[252:253] offset:18448
	v_pk_add_f32 v[218:219], v[218:219], v[4:5]
	v_pk_fma_f32 v[184:185], v[4:5], v[4:5], v[184:185]
	v_pk_add_f32 v[216:217], v[216:217], v[6:7]
	v_pk_fma_f32 v[166:167], v[6:7], v[6:7], v[166:167]
	v_cvt_pk_f16_f32 v254, v8, v9
	v_cvt_pk_f16_f32 v255, v10, v11
	ds_write_b64 v251, v[254:255] offset:18464
	v_pk_add_f32 v[214:215], v[214:215], v[8:9]
	v_pk_fma_f32 v[164:165], v[8:9], v[8:9], v[164:165]
	v_pk_add_f32 v[204:205], v[204:205], v[10:11]
	v_pk_fma_f32 v[162:163], v[10:11], v[10:11], v[162:163]
	v_cvt_pk_f16_f32 v252, v12, v13
	v_cvt_pk_f16_f32 v253, v14, v15
	ds_write_b64 v251, v[252:253] offset:18480
	v_pk_add_f32 v[202:203], v[202:203], v[12:13]
	v_pk_fma_f32 v[160:161], v[12:13], v[12:13], v[160:161]
	v_pk_add_f32 v[196:197], v[196:197], v[14:15]
	v_pk_fma_f32 v[156:157], v[14:15], v[14:15], v[156:157]
	v_cvt_pk_f16_f32 v254, v16, v17
	v_cvt_pk_f16_f32 v255, v18, v19
	ds_write_b64 v251, v[254:255] offset:23040
	v_pk_add_f32 v[222:223], v[222:223], v[16:17]
	v_pk_fma_f32 v[194:195], v[16:17], v[16:17], v[194:195]
	v_pk_add_f32 v[220:221], v[220:221], v[18:19]
	v_pk_fma_f32 v[192:193], v[18:19], v[18:19], v[192:193]
	v_cvt_pk_f16_f32 v252, v20, v21
	v_cvt_pk_f16_f32 v253, v22, v23
	ds_write_b64 v251, v[252:253] offset:23056
	v_pk_add_f32 v[218:219], v[218:219], v[20:21]
	v_pk_fma_f32 v[184:185], v[20:21], v[20:21], v[184:185]
	v_pk_add_f32 v[216:217], v[216:217], v[22:23]
	v_pk_fma_f32 v[166:167], v[22:23], v[22:23], v[166:167]
	v_cvt_pk_f16_f32 v254, v24, v25
	v_cvt_pk_f16_f32 v255, v26, v27
	ds_write_b64 v251, v[254:255] offset:23072
	v_pk_add_f32 v[214:215], v[214:215], v[24:25]
	v_pk_fma_f32 v[164:165], v[24:25], v[24:25], v[164:165]
	v_pk_add_f32 v[204:205], v[204:205], v[26:27]
	v_pk_fma_f32 v[162:163], v[26:27], v[26:27], v[162:163]
	v_cvt_pk_f16_f32 v252, v28, v29
	v_cvt_pk_f16_f32 v253, v30, v31
	ds_write_b64 v251, v[252:253] offset:23088
	v_pk_add_f32 v[202:203], v[202:203], v[28:29]
	v_pk_fma_f32 v[160:161], v[28:29], v[28:29], v[160:161]
	v_pk_add_f32 v[196:197], v[196:197], v[30:31]
	v_pk_fma_f32 v[156:157], v[30:31], v[30:31], v[156:157]
	s_nop 4
	s_nop 0
	v_add_f32_dpp v222, v222, v222 row_half_mirror row_mask:0xf bank_mask:0x5
	v_add_f32_dpp v222, v223, v223 row_half_mirror row_mask:0xf bank_mask:0xa
	v_add_f32_dpp v220, v220, v220 row_half_mirror row_mask:0xf bank_mask:0x5
	v_add_f32_dpp v220, v221, v221 row_half_mirror row_mask:0xf bank_mask:0xa
	v_add_f32_dpp v218, v218, v218 row_half_mirror row_mask:0xf bank_mask:0x5
	v_add_f32_dpp v218, v219, v219 row_half_mirror row_mask:0xf bank_mask:0xa
	v_add_f32_dpp v216, v216, v216 row_half_mirror row_mask:0xf bank_mask:0x5
	v_add_f32_dpp v216, v217, v217 row_half_mirror row_mask:0xf bank_mask:0xa
	v_add_f32_dpp v214, v214, v214 row_half_mirror row_mask:0xf bank_mask:0x5
	v_add_f32_dpp v214, v215, v215 row_half_mirror row_mask:0xf bank_mask:0xa
	v_add_f32_dpp v204, v204, v204 row_half_mirror row_mask:0xf bank_mask:0x5
	v_add_f32_dpp v204, v205, v205 row_half_mirror row_mask:0xf bank_mask:0xa
	v_add_f32_dpp v202, v202, v202 row_half_mirror row_mask:0xf bank_mask:0x5
	v_add_f32_dpp v202, v203, v203 row_half_mirror row_mask:0xf bank_mask:0xa
	v_add_f32_dpp v196, v196, v196 row_half_mirror row_mask:0xf bank_mask:0x5
	v_add_f32_dpp v196, v197, v197 row_half_mirror row_mask:0xf bank_mask:0xa
	v_add_f32_dpp v194, v194, v194 row_half_mirror row_mask:0xf bank_mask:0x5
	v_add_f32_dpp v194, v195, v195 row_half_mirror row_mask:0xf bank_mask:0xa
	v_add_f32_dpp v192, v192, v192 row_half_mirror row_mask:0xf bank_mask:0x5
	v_add_f32_dpp v192, v193, v193 row_half_mirror row_mask:0xf bank_mask:0xa
	v_add_f32_dpp v184, v184, v184 row_half_mirror row_mask:0xf bank_mask:0x5
	v_add_f32_dpp v184, v185, v185 row_half_mirror row_mask:0xf bank_mask:0xa
	v_add_f32_dpp v166, v166, v166 row_half_mirror row_mask:0xf bank_mask:0x5
	v_add_f32_dpp v166, v167, v167 row_half_mirror row_mask:0xf bank_mask:0xa
	v_add_f32_dpp v164, v164, v164 row_half_mirror row_mask:0xf bank_mask:0x5
	v_add_f32_dpp v164, v165, v165 row_half_mirror row_mask:0xf bank_mask:0xa
	v_add_f32_dpp v162, v162, v162 row_half_mirror row_mask:0xf bank_mask:0x5
	v_add_f32_dpp v162, v163, v163 row_half_mirror row_mask:0xf bank_mask:0xa
	v_add_f32_dpp v160, v160, v160 row_half_mirror row_mask:0xf bank_mask:0x5
	v_add_f32_dpp v160, v161, v161 row_half_mirror row_mask:0xf bank_mask:0xa
	v_add_f32_dpp v156, v156, v156 row_half_mirror row_mask:0xf bank_mask:0x5
	v_add_f32_dpp v156, v157, v157 row_half_mirror row_mask:0xf bank_mask:0xa
	v_add_f32_dpp v222, v222, v222 row_ror:8 row_mask:0xf bank_mask:0x3
	v_add_f32_dpp v222, v220, v220 row_ror:8 row_mask:0xf bank_mask:0xc
	v_add_f32_dpp v218, v218, v218 row_ror:8 row_mask:0xf bank_mask:0x3
	v_add_f32_dpp v218, v216, v216 row_ror:8 row_mask:0xf bank_mask:0xc
	v_add_f32_dpp v214, v214, v214 row_ror:8 row_mask:0xf bank_mask:0x3
	v_add_f32_dpp v214, v204, v204 row_ror:8 row_mask:0xf bank_mask:0xc
	v_add_f32_dpp v202, v202, v202 row_ror:8 row_mask:0xf bank_mask:0x3
	v_add_f32_dpp v202, v196, v196 row_ror:8 row_mask:0xf bank_mask:0xc
	v_add_f32_dpp v194, v194, v194 row_ror:8 row_mask:0xf bank_mask:0x3
	v_add_f32_dpp v194, v192, v192 row_ror:8 row_mask:0xf bank_mask:0xc
	v_add_f32_dpp v184, v184, v184 row_ror:8 row_mask:0xf bank_mask:0x3
	v_add_f32_dpp v184, v166, v166 row_ror:8 row_mask:0xf bank_mask:0xc
	v_add_f32_dpp v164, v164, v164 row_ror:8 row_mask:0xf bank_mask:0x3
	v_add_f32_dpp v164, v162, v162 row_ror:8 row_mask:0xf bank_mask:0xc
	v_add_f32_dpp v160, v160, v160 row_ror:8 row_mask:0xf bank_mask:0x3
	v_add_f32_dpp v160, v156, v156 row_ror:8 row_mask:0xf bank_mask:0xc
	v_add_f32_dpp v222, v222, v222 quad_perm:[1,0,3,2] row_mask:0xf bank_mask:0xf
	v_add_f32_dpp v218, v218, v218 quad_perm:[1,0,3,2] row_mask:0xf bank_mask:0xf
	v_add_f32_dpp v214, v214, v214 quad_perm:[1,0,3,2] row_mask:0xf bank_mask:0xf
	v_add_f32_dpp v202, v202, v202 quad_perm:[1,0,3,2] row_mask:0xf bank_mask:0xf
	v_add_f32_dpp v194, v194, v194 quad_perm:[1,0,3,2] row_mask:0xf bank_mask:0xf
	v_add_f32_dpp v184, v184, v184 quad_perm:[1,0,3,2] row_mask:0xf bank_mask:0xf
	v_add_f32_dpp v164, v164, v164 quad_perm:[1,0,3,2] row_mask:0xf bank_mask:0xf
	v_add_f32_dpp v160, v160, v160 quad_perm:[1,0,3,2] row_mask:0xf bank_mask:0xf
	v_add_f32_dpp v222, v222, v222 quad_perm:[2,3,0,1] row_mask:0xf bank_mask:0xf
	v_add_f32_dpp v218, v218, v218 quad_perm:[2,3,0,1] row_mask:0xf bank_mask:0xf
	v_add_f32_dpp v214, v214, v214 quad_perm:[2,3,0,1] row_mask:0xf bank_mask:0xf
	v_add_f32_dpp v202, v202, v202 quad_perm:[2,3,0,1] row_mask:0xf bank_mask:0xf
	v_add_f32_dpp v194, v194, v194 quad_perm:[2,3,0,1] row_mask:0xf bank_mask:0xf
	v_add_f32_dpp v184, v184, v184 quad_perm:[2,3,0,1] row_mask:0xf bank_mask:0xf
	v_add_f32_dpp v164, v164, v164 quad_perm:[2,3,0,1] row_mask:0xf bank_mask:0xf
	v_add_f32_dpp v160, v160, v160 quad_perm:[2,3,0,1] row_mask:0xf bank_mask:0xf
	s_mov_b32 exec_lo, 0x11111111
	s_mov_b32 exec_hi, 0x11111111
	ds_add_f32 v250, v222 offset:0
	ds_add_f32 v250, v218 offset:32
	ds_add_f32 v250, v214 offset:64
	ds_add_f32 v250, v202 offset:96
	ds_add_f32 v250, v194 offset:256
	ds_add_f32 v250, v184 offset:288
	ds_add_f32 v250, v164 offset:320
	ds_add_f32 v250, v160 offset:352
	s_mov_b64 exec, -1
	s_waitcnt lgkmcnt(0)
	s_barrier
	s_cmp_lg_u32 s50, 0
	s_cbranch_scc1 .LBB3_27
	v_mbcnt_lo_u32_b32 v2, -1, 0
	v_mbcnt_hi_u32_b32 v2, -1, v2
	v_and_b32_e32 v3, 32, v2
	v_add_u32_e32 v4, v2, v3
	v_lshl_add_u32 v5, v4, 2, s49
	ds_read_b32 v6, v5
	v_lshl_add_u32 v4, v3, 1, v4
	v_add_u32_e32 v4, s48, v4
	v_lshlrev_b32_e32 v4, 2, v4
	s_waitcnt lgkmcnt(0)
	global_atomic_add_f32 v4, v6, s[46:47]
